# attention loops: m0 save/restore around each LDS-DMA removed (m0 has no other reader; every DMA sets it)
# baseline (speedup 1.0000x reference)
.LBB0_676:
	s_lshl_b32 s6, s29, 8
	s_ashr_i32 s14, s29, 7
	s_and_b32 s6, s6, 0xf00
	s_lshr_b32 s8, s29, 4
	s_bfe_u32 s30, s29, 0x30004
	s_mul_i32 s5, s14, 0x2100
	s_addk_i32 s6, 0x100
	s_mul_hi_i32 s4, s14, 0x2100
	s_add_u32 s6, s5, s6
	s_addc_u32 s7, s4, 0
	s_lshl_b64 s[4:5], s[6:7], 8
	s_add_u32 s4, s20, s4
	s_addc_u32 s5, s21, s5
	s_lshl_b32 s9, s30, 5
	s_add_u32 s4, s4, s9
	s_addc_u32 s5, s5, 0
	s_mul_i32 s10, s14, 0x84000
	s_mul_hi_i32 s9, s14, 0x84000
	s_add_u32 s10, s22, s10
	s_addc_u32 s9, s23, s9
	s_bfe_u32 s15, s8, 0x10002
	s_lshl_b32 s8, s15, 5
	v_mov_b32_e32 v201, v0
	s_add_u32 s10, s10, s8
	s_addc_u32 s11, s9, 0
	v_readfirstlane_b32 s34, v201
	s_ashr_i32 s9, s34, 6
	v_and_b32_e32 v202, 31, v201
	s_lshl_b32 s8, s9, 5
	v_or_b32_e32 v18, s8, v202
	v_ashrrev_i32_e32 v19, 31, v18
	v_bfe_u32 v203, v201, 5, 1
	v_lshlrev_b64 v[18:19], 8, v[18:19]
	v_lshl_add_u64 v[18:19], s[4:5], 0, v[18:19]
	v_lshlrev_b32_e32 v194, 4, v203
	v_mov_b32_e32 v195, v219
	v_lshl_add_u64 v[18:19], v[18:19], 0, v[194:195]
	global_load_dwordx4 v[174:177], v[18:19], off
	v_add_co_u32_e32 v18, vcc, s97, v18
	s_waitcnt vmcnt(0)
	s_bfe_u32 s31, s34, 0x10007
	v_addc_co_u32_e32 v19, vcc, 0, v19, vcc
	global_load_dwordx4 v[178:181], v[18:19], off
	s_and_b32 s4, s9, 1
	s_lshl_b32 s5, s31, 11
	v_and_b32_e32 v195, 63, v201
	s_lshl_b32 s12, s4, 10
	s_add_i32 s33, s5, s17
	v_lshlrev_b32_e32 v18, 6, v195
	s_add_i32 s33, s33, s12
	v_lshl_or_b32 v18, s31, 12, v18
	s_cmp_lt_i32 s9, 4
	v_lshl_or_b32 v218, s4, 4, v18
	s_cselect_b64 s[12:13], -1, 0
	s_cmp_gt_i32 s9, 3
	v_lshl_add_u64 v[196:197], s[10:11], 0, v[218:219]
	s_cselect_b64 s[10:11], -1, 0
	s_and_b64 vcc, exec, s[10:11]
	s_waitcnt vmcnt(0)
	s_cbranch_vccnz .LBB0_678
	s_mov_b32 m0, s33
	s_nop 0
	global_load_lds_dwordx4 v[196:197], off
.LBB0_678:
	v_cndmask_b32_e64 v18, 0, 1, s[12:13]
	v_cmp_ne_u32_e64 s[4:5], 1, v18
	s_andn2_b64 vcc, exec, s[12:13]
	s_cbranch_vccnz .LBB0_680
	s_mov_b64 s[12:13], 0x2000
	v_lshl_add_u64 v[18:19], v[196:197], 0, s[12:13]
	s_add_i32 s12, s33, 0x1000
	s_mov_b32 m0, s12
	s_nop 0
	global_load_lds_dwordx4 v[18:19], off
.LBB0_680:
	s_lshl_b32 s12, s14, 1
	s_or_b32 s12, s15, s12
	s_ashr_i32 s34, s34, 8
	s_and_b32 s35, s9, 3
	s_mul_hi_i32 s13, s12, 0x84000
	s_mul_i32 s12, s12, 0x84000
	v_mul_u32_u24_e32 v18, 0x2100, v195
	s_add_u32 s12, s24, s12
	v_lshl_add_u32 v18, s34, 6, v18
	s_addc_u32 s13, s25, s13
	s_lshl_b32 s14, s34, 12
	v_lshl_or_b32 v218, s35, 4, v18
	s_lshl_b32 s15, s35, 10
	s_add_i32 s35, s28, s14
	s_min_i32 s14, s34, 0x83
	s_sub_i32 s14, s14, s34
	s_add_i32 s35, s35, s15
	s_ashr_i32 s15, s14, 31
	s_lshl_b64 s[14:15], s[14:15], 6
	s_add_u32 s14, s12, s14
	s_addc_u32 s15, s13, s15
	v_lshl_add_u64 v[18:19], s[14:15], 0, v[218:219]
	s_mov_b32 m0, s35
	s_nop 0
	global_load_lds_dwordx4 v[18:19], off
	s_and_b64 vcc, exec, s[4:5]
	s_cbranch_vccnz .LBB0_682
	s_mov_b64 s[14:15], 0x4000
	v_lshl_add_u64 v[18:19], v[196:197], 0, s[14:15]
	s_add_i32 s14, s33, 0x2000
	s_mov_b32 m0, s14
	s_nop 0
	global_load_lds_dwordx4 v[18:19], off
.LBB0_682:
	s_min_i32 s14, s34, 0x81
	s_sub_i32 s14, s14, s34
	s_ashr_i32 s15, s14, 31
	s_lshl_b64 s[14:15], s[14:15], 6
	s_add_u32 s14, s12, s14
	s_addc_u32 s15, s13, s15
	v_lshl_add_u64 v[18:19], s[14:15], 0, v[218:219]
	v_lshl_add_u64 v[18:19], v[18:19], 0, s[72:73]
	s_add_i32 s14, s35, 0x2000
	s_mov_b32 m0, s14
	s_nop 0
	global_load_lds_dwordx4 v[18:19], off
	s_mov_b64 s[14:15], -1
	s_and_b64 vcc, exec, s[10:11]
	s_cbranch_vccz .LBB0_684
	s_waitcnt vmcnt(1) lgkmcnt(0)
	s_barrier
	s_mov_b64 s[14:15], 0

.LBB0_686:
	v_lshlrev_b32_e32 v19, 10, v203
	v_lshlrev_b32_e32 v18, 4, v202
	v_add3_u32 v205, s17, v19, v18
	ds_read_b128 v[50:53], v205
	ds_read_b128 v[54:57], v205 offset:512
	s_waitcnt lgkmcnt(0)
	s_barrier
	s_and_b64 vcc, exec, s[4:5]
	s_cbranch_vccnz .LBB0_688
	s_mov_b64 s[14:15], 0x6000
	v_lshl_add_u64 v[20:21], v[196:197], 0, s[14:15]
	s_add_i32 s14, s33, 0x3000
	s_mov_b32 m0, s14
	s_nop 0
	global_load_lds_dwordx4 v[20:21], off
.LBB0_688:
	s_min_i32 s14, s34, 0x7f
	s_sub_i32 s14, s14, s34
	s_ashr_i32 s15, s14, 31
	v_lshrrev_b32_e32 v19, 4, v201
	v_lshrrev_b32_e32 v20, 3, v201
	s_lshl_b64 s[14:15], s[14:15], 6
	v_bitop3_b32 v19, v19, 1, v20 bitop3:0x48
	s_add_u32 s14, s12, s14
	v_cmp_eq_u32_e32 vcc, 0, v19
	v_lshlrev_b32_e32 v19, 11, v203
	s_addc_u32 s15, s13, s15
	v_add3_u32 v206, s17, v19, v18
	v_lshl_add_u64 v[18:19], s[14:15], 0, v[218:219]
	v_lshl_add_u64 v[18:19], v[18:19], 0, s[76:77]
	s_add_i32 s14, s35, 0x4000
	s_mov_b32 m0, s14
	s_nop 0
	global_load_lds_dwordx4 v[18:19], off
	v_cndmask_b32_e32 v114, 0, v237, vcc
	v_mov_b32_e32 v115, v114
	v_mov_b32_e32 v116, v114
	v_mov_b32_e32 v117, v114
	v_mov_b32_e32 v118, v114
	v_mov_b32_e32 v119, v114
	v_mov_b32_e32 v120, v114
	v_mov_b32_e32 v121, v114
	v_mov_b32_e32 v204, 0x7f7f7f7f
	v_mov_b32_e32 v207, 0x76767676
	v_mov_b32_e32 v208, 0x7e7e7e7e
	s_waitcnt lgkmcnt(1)
	v_mfma_scale_f32_32x32x64_f8f6f4 v[34:49], v[50:53], v[174:177], v[2:17], v208, v207 op_sel_hi:[0,0,0] cbsz:4 blgp:4
	s_waitcnt lgkmcnt(0)
	v_mfma_scale_f32_32x32x64_f8f6f4 v[18:33], v[54:57], v[174:177], v[2:17], v208, v207 op_sel_hi:[0,0,0] cbsz:4 blgp:4
	s_nop 0
	s_nop 15
	s_nop 15
	s_nop 0
	v_cvt_pknorm_u16_f32 v18, v18, v19
	v_cvt_pknorm_u16_f32 v19, v20, v21
	v_perm_b32 v126, v19, v18, s86
	v_cvt_pknorm_u16_f32 v18, v38, v39
	v_cvt_pknorm_u16_f32 v19, v40, v41
	v_perm_b32 v123, v19, v18, s86
	v_cvt_pknorm_u16_f32 v18, v22, v23
	v_cvt_pknorm_u16_f32 v19, v24, v25
	v_perm_b32 v127, v19, v18, s86
	v_cvt_pknorm_u16_f32 v18, v42, v43
	v_cvt_pknorm_u16_f32 v19, v44, v45
	v_perm_b32 v124, v19, v18, s86
	v_cvt_pknorm_u16_f32 v18, v26, v27
	v_cvt_pknorm_u16_f32 v19, v28, v29
	v_perm_b32 v128, v19, v18, s86
	v_cvt_pknorm_u16_f32 v18, v46, v47
	v_cvt_pknorm_u16_f32 v19, v48, v49
	v_cvt_pknorm_u16_f32 v34, v34, v35
	v_cvt_pknorm_u16_f32 v35, v36, v37
	v_perm_b32 v125, v19, v18, s86
	v_cvt_pknorm_u16_f32 v18, v30, v31
	v_cvt_pknorm_u16_f32 v19, v32, v33
	v_perm_b32 v122, v35, v34, s86
	v_perm_b32 v129, v19, v18, s86
	v_mfma_scale_f32_32x32x64_f8f6f4 v[34:49], v[50:53], v[178:181], v[2:17], v208, v207 op_sel_hi:[0,0,0] cbsz:4 blgp:4
	v_mfma_scale_f32_32x32x64_f8f6f4 v[18:33], v[54:57], v[178:181], v[2:17], v208, v207 op_sel_hi:[0,0,0] cbsz:4 blgp:4
	s_nop 0
	s_nop 15
	s_nop 15
	s_nop 0
	v_cvt_pknorm_u16_f32 v18, v18, v19
	v_cvt_pknorm_u16_f32 v19, v20, v21
	v_perm_b32 v134, v19, v18, s86
	v_cvt_pknorm_u16_f32 v18, v38, v39
	v_cvt_pknorm_u16_f32 v19, v40, v41
	v_perm_b32 v131, v19, v18, s86
	v_cvt_pknorm_u16_f32 v18, v22, v23
	v_cvt_pknorm_u16_f32 v19, v24, v25
	v_perm_b32 v135, v19, v18, s86
	v_cvt_pknorm_u16_f32 v18, v42, v43
	v_cvt_pknorm_u16_f32 v19, v44, v45
	v_perm_b32 v132, v19, v18, s86
	v_cvt_pknorm_u16_f32 v18, v26, v27
	v_cvt_pknorm_u16_f32 v19, v28, v29
	v_perm_b32 v136, v19, v18, s86
	v_cvt_pknorm_u16_f32 v18, v46, v47
	v_cvt_pknorm_u16_f32 v19, v48, v49
	v_cvt_pknorm_u16_f32 v34, v34, v35
	v_cvt_pknorm_u16_f32 v35, v36, v37
	v_perm_b32 v133, v19, v18, s86
	v_cvt_pknorm_u16_f32 v18, v30, v31
	v_cvt_pknorm_u16_f32 v19, v32, v33
	v_perm_b32 v130, v35, v34, s86
	v_perm_b32 v137, v19, v18, s86
	ds_read_b128 v[186:189], v205 offset:2048
	ds_read_b128 v[190:193], v205 offset:2560
	s_setprio 1
	s_waitcnt lgkmcnt(1)
	v_mfma_scale_f32_32x32x64_f8f6f4 v[74:89], v[186:189], v[174:177], v[2:17], v208, v207 op_sel_hi:[0,0,0] cbsz:4 blgp:4
	s_waitcnt lgkmcnt(0)
	v_mfma_scale_f32_32x32x64_f8f6f4 v[34:49], v[190:193], v[174:177], v[2:17], v208, v207 op_sel_hi:[0,0,0] cbsz:4 blgp:4
	ds_read_b128 v[154:157], v206 offset:16384
	ds_read_b128 v[162:165], v206 offset:16896
	ds_read_b128 v[158:161], v206 offset:17408
	ds_read_b128 v[166:169], v206 offset:17920
	v_readlane_b32 s40, v255, 8
	v_readlane_b32 s41, v255, 9
	v_readlane_b32 s42, v255, 10
	v_readlane_b32 s43, v255, 11
	v_readlane_b32 s44, v255, 12
	v_readlane_b32 s45, v255, 13
	v_readlane_b32 s46, v255, 14
	v_readlane_b32 s47, v255, 15
	v_readlane_b32 s48, v255, 16
	v_readlane_b32 s49, v255, 17
	v_readlane_b32 s50, v255, 18
	v_readlane_b32 s51, v255, 19
	v_readlane_b32 s52, v255, 20
	v_readlane_b32 s53, v255, 21
	v_readlane_b32 s54, v255, 22
	v_readlane_b32 s55, v255, 23
	v_mov_b64_e32 v[18:19], s[40:41]
	v_mov_b64_e32 v[20:21], s[42:43]
	v_mov_b64_e32 v[32:33], s[54:55]
	v_mov_b64_e32 v[22:23], s[44:45]
	v_mov_b64_e32 v[24:25], s[46:47]
	v_mov_b64_e32 v[26:27], s[48:49]
	v_mov_b64_e32 v[28:29], s[50:51]
	v_mov_b64_e32 v[30:31], s[52:53]
	v_mov_b64_e32 v[64:65], v[32:33]
	v_mov_b64_e32 v[62:63], v[30:31]
	v_mov_b64_e32 v[60:61], v[28:29]
	v_mov_b64_e32 v[58:59], v[26:27]
	v_mov_b64_e32 v[56:57], v[24:25]
	v_mov_b64_e32 v[54:55], v[22:23]
	v_mov_b64_e32 v[52:53], v[20:21]
	v_mov_b64_e32 v[50:51], v[18:19]
	s_waitcnt lgkmcnt(1)
	v_mfma_scale_f32_32x32x64_f8f6f4 v[50:65], v[122:129], v[154:161], v[50:65], v204, v204 op_sel_hi:[0,0,0] cbsz:1
	s_setprio 0
	s_nop 15
	s_nop 5
	s_nop 0
	v_cvt_pknorm_u16_f32 v34, v34, v35
	v_cvt_pknorm_u16_f32 v35, v36, v37
	v_perm_b32 v142, v35, v34, s86
	v_cvt_pknorm_u16_f32 v34, v78, v79
	v_cvt_pknorm_u16_f32 v35, v80, v81
	v_cvt_pknorm_u16_f32 v66, v74, v75
	v_cvt_pknorm_u16_f32 v67, v76, v77
	v_perm_b32 v139, v35, v34, s86
	v_cvt_pknorm_u16_f32 v34, v38, v39
	v_cvt_pknorm_u16_f32 v35, v40, v41
	v_perm_b32 v138, v67, v66, s86
	v_perm_b32 v143, v35, v34, s86
	v_mov_b64_e32 v[80:81], v[32:33]
	v_mov_b64_e32 v[78:79], v[30:31]
	v_mov_b64_e32 v[76:77], v[28:29]
	v_mov_b64_e32 v[74:75], v[26:27]
	v_mov_b64_e32 v[72:73], v[24:25]
	v_mov_b64_e32 v[70:71], v[22:23]
	v_mov_b64_e32 v[68:69], v[20:21]
	v_mov_b64_e32 v[66:67], v[18:19]
	s_waitcnt lgkmcnt(0)
	v_mfma_scale_f32_32x32x64_f8f6f4 v[66:81], v[122:129], v[162:169], v[66:81], v204, v204 op_sel_hi:[0,0,0] cbsz:1
	v_cvt_pknorm_u16_f32 v34, v82, v83
	v_cvt_pknorm_u16_f32 v35, v84, v85
	v_perm_b32 v140, v35, v34, s86
	v_cvt_pknorm_u16_f32 v34, v42, v43
	v_cvt_pknorm_u16_f32 v35, v44, v45
	v_perm_b32 v144, v35, v34, s86
	v_cvt_pknorm_u16_f32 v34, v86, v87
	v_cvt_pknorm_u16_f32 v35, v88, v89
	v_perm_b32 v141, v35, v34, s86
	v_cvt_pknorm_u16_f32 v34, v46, v47
	v_cvt_pknorm_u16_f32 v35, v48, v49
	v_perm_b32 v145, v35, v34, s86
	v_mov_b64_e32 v[172:173], s[90:91]
	v_mov_b64_e32 v[184:185], s[90:91]
	v_mov_b64_e32 v[170:171], s[88:89]
	v_mov_b64_e32 v[182:183], s[88:89]
	v_mfma_scale_f32_16x16x128_f8f6f4 v[182:185], v[122:129], v[114:121], v[182:185], v204, v204 op_sel_hi:[0,0,0] cbsz:1
	s_setprio 1
	v_mfma_scale_f32_32x32x64_f8f6f4 v[98:113], v[186:189], v[178:181], v[2:17], v208, v207 op_sel_hi:[0,0,0] cbsz:4 blgp:4
	v_mfma_scale_f32_32x32x64_f8f6f4 v[82:97], v[190:193], v[178:181], v[2:17], v208, v207 op_sel_hi:[0,0,0] cbsz:4 blgp:4
	v_mov_b64_e32 v[48:49], v[32:33]
	v_mov_b64_e32 v[46:47], v[30:31]
	v_mov_b64_e32 v[44:45], v[28:29]
	v_mov_b64_e32 v[42:43], v[26:27]
	v_mov_b64_e32 v[40:41], v[24:25]
	v_mov_b64_e32 v[38:39], v[22:23]
	v_mov_b64_e32 v[36:37], v[20:21]
	v_mov_b64_e32 v[34:35], v[18:19]
	v_mfma_scale_f32_32x32x64_f8f6f4 v[34:49], v[130:137], v[154:161], v[34:49], v204, v204 op_sel_hi:[0,0,0] cbsz:1
	s_setprio 0
	s_nop 15
	s_nop 5
	s_nop 0
	v_cvt_pknorm_u16_f32 v82, v82, v83
	v_cvt_pknorm_u16_f32 v83, v84, v85
	v_perm_b32 v150, v83, v82, s86
	v_cvt_pknorm_u16_f32 v82, v102, v103
	v_cvt_pknorm_u16_f32 v83, v104, v105
	v_cvt_pknorm_u16_f32 v98, v98, v99
	v_cvt_pknorm_u16_f32 v99, v100, v101
	v_perm_b32 v147, v83, v82, s86
	v_cvt_pknorm_u16_f32 v82, v86, v87
	v_cvt_pknorm_u16_f32 v83, v88, v89
	v_perm_b32 v146, v99, v98, s86
	v_perm_b32 v151, v83, v82, s86
	v_mfma_scale_f32_32x32x64_f8f6f4 v[18:33], v[130:137], v[162:169], v[18:33], v204, v204 op_sel_hi:[0,0,0] cbsz:1
	ds_read_b128 v[186:189], v205 offset:4096
	ds_read_b128 v[190:193], v205 offset:4608
	v_cvt_pknorm_u16_f32 v82, v106, v107
	v_cvt_pknorm_u16_f32 v83, v108, v109
	v_perm_b32 v148, v83, v82, s86
	v_cvt_pknorm_u16_f32 v82, v90, v91
	v_cvt_pknorm_u16_f32 v83, v92, v93
	v_perm_b32 v152, v83, v82, s86
	v_cvt_pknorm_u16_f32 v82, v110, v111
	v_cvt_pknorm_u16_f32 v83, v112, v113
	v_perm_b32 v149, v83, v82, s86
	v_cvt_pknorm_u16_f32 v82, v94, v95
	v_cvt_pknorm_u16_f32 v83, v96, v97
	v_perm_b32 v153, v83, v82, s86
	v_mfma_scale_f32_16x16x128_f8f6f4 v[170:173], v[130:137], v[114:121], v[170:173], v204, v204 op_sel_hi:[0,0,0] cbsz:1
	s_mov_b64 s[14:15], -1
	s_and_b64 vcc, exec, s[10:11]
	s_cbranch_vccz .LBB0_700
	s_waitcnt vmcnt(1) lgkmcnt(0)
	s_barrier
	s_cbranch_execz .LBB0_701

.LBB0_691:
	v_lshl_add_u64 v[82:83], v[196:197], 0, s[68:69]
	s_mov_b32 m0, s33
	s_nop 0
	global_load_lds_dwordx4 v[82:83], off
.LBB0_692:
	s_min_i32 s14, s34, 0x7d
	s_sub_i32 s14, s14, s34
	s_ashr_i32 s15, s14, 31
	s_lshl_b64 s[14:15], s[14:15], 6
	s_add_u32 s14, s12, s14
	s_addc_u32 s15, s13, s15
	v_lshl_add_u64 v[82:83], s[14:15], 0, v[218:219]
	s_mov_b64 s[14:15], 0x180
	v_lshl_add_u64 v[82:83], v[82:83], 0, s[14:15]
	s_add_i32 s14, s35, 0x6000
	s_mov_b32 m0, s14
	s_nop 0
	global_load_lds_dwordx4 v[82:83], off
	v_lshl_add_u64 v[198:199], s[12:13], 0, v[218:219]
	s_or_b32 s14, s31, 10
	s_add_i32 s15, s34, 8
	s_mov_b32 s36, 1
	s_mov_b32 s38, 0x8000
	s_movk_i32 s39, 0x2000
	s_branch .LBB0_694
.LBB0_693:
	s_min_i32 s12, s15, 0x83
	s_sub_i32 s12, s12, s34
	s_ashr_i32 s13, s12, 31
	s_lshl_b64 s[12:13], s[12:13], 6
	v_lshl_add_u64 v[82:83], v[198:199], 0, s[12:13]
	s_add_i32 s12, s40, s35
	s_mov_b32 m0, s12
	s_nop 0
	global_load_lds_dwordx4 v[82:83], off
	s_add_i32 s14, s14, 2
	s_addk_i32 s38, 0x2000
	s_addk_i32 s39, 0x1000
	s_add_i32 s15, s15, 2
	s_add_i32 s36, s36, 1
	s_cmp_eq_u32 s39, 0x43000
	s_cbranch_scc1 .LBB0_702

.LBB0_699:
	s_min_i32 s12, s14, 0x83
	s_sub_i32 s12, s12, s31
	s_ashr_i32 s13, s12, 31
	s_lshl_b64 s[12:13], s[12:13], 12
	v_lshl_add_u64 v[82:83], v[196:197], 0, s[12:13]
	s_add_i32 s12, s39, 0xfffff000
	s_and_b32 s12, s12, 0x3000
	s_add_i32 s12, s12, s33
	s_mov_b32 m0, s12
	s_nop 0
	global_load_lds_dwordx4 v[82:83], off
	s_branch .LBB0_693

.LBB0_709:
	s_ashr_i32 s25, s16, 3
	s_and_b32 s24, s16, 7
	s_mul_i32 s3, s25, 0x210000
	s_mul_hi_i32 s2, s25, 0x210000
	s_add_u32 s3, s12, s3
	s_addc_u32 s2, s13, s2
	s_lshl_b32 s4, s24, 5
	s_add_u32 s4, s3, s4
	s_addc_u32 s5, s2, 0
	s_mul_i32 s3, s25, 0x84000
	s_mul_hi_i32 s2, s25, 0x84000
	s_add_u32 s3, s14, s3
	s_addc_u32 s2, s15, s2
	s_bfe_u32 s28, s16, 0x10002
	s_lshl_b32 s6, s28, 5
	v_mov_b32_e32 v142, v0
	s_add_u32 s6, s3, s6
	s_addc_u32 s7, s2, 0
	v_readfirstlane_b32 s27, v142
	s_ashr_i32 s3, s27, 6
	v_and_b32_e32 v143, 31, v142
	s_lshl_b32 s2, s3, 5
	v_or_b32_e32 v18, s2, v143
	v_ashrrev_i32_e32 v19, 31, v18
	v_bfe_u32 v144, v142, 5, 1
	v_lshlrev_b64 v[18:19], 8, v[18:19]
	v_lshl_add_u64 v[18:19], s[4:5], 0, v[18:19]
	v_lshlrev_b32_e32 v138, 4, v144
	v_mov_b32_e32 v139, v219
	v_lshl_add_u64 v[18:19], v[18:19], 0, v[138:139]
	global_load_dwordx4 v[122:125], v[18:19], off
	s_bfe_u32 s33, s27, 0x10007
	s_and_b32 s4, s3, 1
	s_lshl_b32 s5, s33, 11
	s_lshl_b32 s8, s4, 4
	s_add_i32 s5, s5, s17
	s_lshl_b32 s4, s4, 10
	s_lshl_b32 s31, s33, 6
	s_add_i32 s26, s5, s4
	v_and_b32_e32 v139, 63, v142
	s_cmp_lt_i32 s3, 4
	v_or_b32_e32 v18, s31, v139
	s_cselect_b64 s[10:11], -1, 0
	s_cmp_gt_i32 s3, 3
	v_lshl_or_b32 v218, v18, 6, s8
	s_cselect_b64 s[8:9], -1, 0
	v_lshl_add_u64 v[18:19], s[6:7], 0, v[218:219]
	s_and_b64 vcc, exec, s[8:9]
	s_waitcnt vmcnt(0)
	s_cbranch_vccnz .LBB0_711
	s_mov_b32 m0, s26
	s_nop 0
	global_load_lds_dwordx4 v[18:19], off
.LBB0_711:
	v_cndmask_b32_e64 v20, 0, 1, s[10:11]
	v_cmp_ne_u32_e64 s[4:5], 1, v20
	s_andn2_b64 vcc, exec, s[10:11]
	s_cbranch_vccnz .LBB0_713
	s_mov_b64 s[10:11], 0x2000
	v_lshl_add_u64 v[18:19], v[18:19], 0, s[10:11]
	s_add_i32 s10, s26, 0x1000
	s_mov_b32 m0, s10
	s_nop 0
	global_load_lds_dwordx4 v[18:19], off
.LBB0_713:
	s_lshl_b32 s11, s25, 1
	s_or_b32 s11, s11, s28
	s_ashr_i32 s27, s27, 8
	s_and_b32 s10, s3, 3
	s_mul_hi_i32 s28, s11, 0x84000
	s_mul_i32 s11, s11, 0x84000
	v_mul_u32_u24_e32 v18, 0x2100, v139
	s_add_u32 s29, s19, s11
	v_lshl_add_u32 v18, s27, 6, v18
	s_addc_u32 s30, s20, s28
	s_lshl_b32 s11, s27, 12
	v_lshl_or_b32 v140, s10, 4, v18
	s_add_i32 s11, s23, s11
	s_lshl_b32 s10, s10, 10
	s_add_i32 s28, s11, s10
	s_min_i32 s10, s27, 3
	s_sub_i32 s10, s10, s27
	s_ashr_i32 s11, s10, 31
	s_lshl_b64 s[10:11], s[10:11], 6
	s_add_u32 s10, s29, s10
	v_mov_b32_e32 v141, v219
	s_addc_u32 s11, s30, s11
	v_lshl_add_u64 v[18:19], s[10:11], 0, v[140:141]
	s_mov_b32 m0, s28
	s_nop 0
	global_load_lds_dwordx4 v[18:19], off
	s_and_b64 vcc, exec, s[4:5]
	s_cbranch_vccnz .LBB0_715
	s_lshl_b32 s10, s33, 12
	s_xor_b32 s10, s10, 0x3000
	s_add_u32 s10, s6, s10
	s_addc_u32 s11, s7, 0
	v_lshl_add_u64 v[18:19], s[10:11], 0, v[218:219]
	s_add_i32 s10, s26, 0x2000
	s_mov_b32 m0, s10
	s_nop 0
	global_load_lds_dwordx4 v[18:19], off
.LBB0_715:
	s_min_i32 s10, s27, 1
	s_sub_i32 s10, s10, s27
	s_ashr_i32 s11, s10, 31
	s_lshl_b64 s[10:11], s[10:11], 6
	s_add_u32 s10, s29, s10
	s_addc_u32 s11, s30, s11
	v_lshl_add_u64 v[18:19], s[10:11], 0, v[140:141]
	v_lshl_add_u64 v[18:19], v[18:19], 0, s[72:73]
	s_add_i32 s10, s28, 0x2000
	s_mov_b32 m0, s10
	s_nop 0
	global_load_lds_dwordx4 v[18:19], off
	s_mov_b64 s[10:11], -1
	s_and_b64 vcc, exec, s[8:9]
	s_cbranch_vccz .LBB0_717
	s_waitcnt vmcnt(1) lgkmcnt(0)
	s_barrier
	s_mov_b64 s[10:11], 0

.LBB0_719:
	v_lshl_add_u32 v18, v144, 10, s17
	v_lshlrev_b32_e32 v98, 4, v143
	v_add_u32_e32 v147, v18, v98
	ds_read_b128 v[50:53], v147
	ds_read_b128 v[54:57], v147 offset:512
	s_waitcnt lgkmcnt(0)
	s_barrier
	s_and_b64 vcc, exec, s[4:5]
	s_cbranch_vccnz .LBB0_721
	s_lshl_b32 s10, s33, 12
	s_xor_b32 s10, s10, 0x3000
	s_add_u32 s10, s6, s10
	s_addc_u32 s11, s7, 0
	v_lshl_add_u64 v[18:19], s[10:11], 0, v[218:219]
	s_add_i32 s10, s26, 0x3000
	s_mov_b32 m0, s10
	s_nop 0
	global_load_lds_dwordx4 v[18:19], off
.LBB0_721:
	s_min_i32 s10, s27, -1
	s_sub_i32 s10, s10, s27
	s_ashr_i32 s11, s10, 31
	s_lshl_b64 s[10:11], s[10:11], 6
	v_lshrrev_b32_e32 v18, 4, v142
	v_lshrrev_b32_e32 v19, 3, v142
	s_add_u32 s10, s29, s10
	v_bitop3_b32 v18, v18, 1, v19 bitop3:0x48
	s_addc_u32 s11, s30, s11
	v_cmp_eq_u32_e32 vcc, 0, v18
	v_lshl_add_u64 v[18:19], s[10:11], 0, v[140:141]
	v_lshl_add_u64 v[18:19], v[18:19], 0, s[76:77]
	s_add_i32 s10, s28, 0x4000
	s_mov_b32 m0, s10
	s_nop 0
	global_load_lds_dwordx4 v[18:19], off
	v_cndmask_b32_e32 v82, 0, v237, vcc
	v_mov_b32_e32 v83, v82
	v_mov_b32_e32 v84, v82
	v_mov_b32_e32 v85, v82
	v_mov_b32_e32 v86, v82
	v_mov_b32_e32 v87, v82
	v_mov_b32_e32 v88, v82
	v_mov_b32_e32 v89, v82
	v_lshl_add_u32 v99, v144, 11, s17
	v_mov_b32_e32 v145, 0x7f7f7f7f
	v_mov_b32_e32 v148, 0x76767676
	v_mov_b32_e32 v149, 0x7e7e7e7e
	s_waitcnt lgkmcnt(1)
	v_mfma_scale_f32_32x32x64_f8f6f4 v[34:49], v[50:53], v[122:125], v[2:17], v149, v148 op_sel_hi:[0,0,0] cbsz:4 blgp:4
	s_waitcnt lgkmcnt(0)
	v_mfma_scale_f32_32x32x64_f8f6f4 v[18:33], v[54:57], v[122:125], v[2:17], v149, v148 op_sel_hi:[0,0,0] cbsz:4 blgp:4
	s_nop 0
	s_nop 15
	s_nop 15
	s_nop 0
	v_cvt_pknorm_u16_f32 v18, v18, v19
	v_cvt_pknorm_u16_f32 v19, v20, v21
	v_perm_b32 v94, v19, v18, s86
	v_cvt_pknorm_u16_f32 v18, v38, v39
	v_cvt_pknorm_u16_f32 v19, v40, v41
	v_perm_b32 v91, v19, v18, s86
	v_cvt_pknorm_u16_f32 v18, v22, v23
	v_cvt_pknorm_u16_f32 v19, v24, v25
	v_perm_b32 v95, v19, v18, s86
	v_cvt_pknorm_u16_f32 v18, v42, v43
	v_cvt_pknorm_u16_f32 v19, v44, v45
	v_perm_b32 v92, v19, v18, s86
	v_cvt_pknorm_u16_f32 v18, v26, v27
	v_cvt_pknorm_u16_f32 v19, v28, v29
	v_perm_b32 v96, v19, v18, s86
	v_cvt_pknorm_u16_f32 v18, v46, v47
	v_cvt_pknorm_u16_f32 v19, v48, v49
	v_cvt_pknorm_u16_f32 v34, v34, v35
	v_cvt_pknorm_u16_f32 v35, v36, v37
	v_perm_b32 v93, v19, v18, s86
	v_cvt_pknorm_u16_f32 v18, v30, v31
	v_cvt_pknorm_u16_f32 v19, v32, v33
	v_perm_b32 v90, v35, v34, s86
	v_perm_b32 v97, v19, v18, s86
	ds_read_b128 v[134:137], v147 offset:2048
	ds_read_b128 v[150:153], v147 offset:2560
	s_setprio 1
	s_waitcnt lgkmcnt(1)
	v_mfma_scale_f32_32x32x64_f8f6f4 v[66:81], v[134:137], v[122:125], v[2:17], v149, v148 op_sel_hi:[0,0,0] cbsz:4 blgp:4
	s_waitcnt lgkmcnt(0)
	v_mfma_scale_f32_32x32x64_f8f6f4 v[50:65], v[150:153], v[122:125], v[2:17], v149, v148 op_sel_hi:[0,0,0] cbsz:4 blgp:4
	v_add_u32_e32 v146, v99, v98
	ds_read_b128 v[106:109], v146 offset:16384
	ds_read_b128 v[114:117], v146 offset:16896
	ds_read_b128 v[110:113], v146 offset:17408
	ds_read_b128 v[118:121], v146 offset:17920
	v_readlane_b32 s40, v255, 8
	v_readlane_b32 s41, v255, 9
	v_readlane_b32 s42, v255, 10
	v_readlane_b32 s43, v255, 11
	v_readlane_b32 s44, v255, 12
	v_readlane_b32 s45, v255, 13
	v_readlane_b32 s46, v255, 14
	v_readlane_b32 s47, v255, 15
	v_readlane_b32 s48, v255, 16
	v_readlane_b32 s49, v255, 17
	v_readlane_b32 s50, v255, 18
	v_readlane_b32 s51, v255, 19
	v_readlane_b32 s52, v255, 20
	v_readlane_b32 s53, v255, 21
	v_readlane_b32 s54, v255, 22
	v_readlane_b32 s55, v255, 23
	v_mov_b64_e32 v[18:19], s[40:41]
	v_mov_b64_e32 v[20:21], s[42:43]
	v_mov_b64_e32 v[32:33], s[54:55]
	v_mov_b64_e32 v[22:23], s[44:45]
	v_mov_b64_e32 v[24:25], s[46:47]
	v_mov_b64_e32 v[26:27], s[48:49]
	v_mov_b64_e32 v[28:29], s[50:51]
	v_mov_b64_e32 v[30:31], s[52:53]
	v_mov_b64_e32 v[48:49], v[32:33]
	v_mov_b64_e32 v[46:47], v[30:31]
	v_mov_b64_e32 v[44:45], v[28:29]
	v_mov_b64_e32 v[42:43], v[26:27]
	v_mov_b64_e32 v[40:41], v[24:25]
	v_mov_b64_e32 v[38:39], v[22:23]
	v_mov_b64_e32 v[36:37], v[20:21]
	v_mov_b64_e32 v[34:35], v[18:19]
	s_waitcnt lgkmcnt(1)
	v_mfma_scale_f32_32x32x64_f8f6f4 v[34:49], v[90:97], v[106:113], v[34:49], v145, v145 op_sel_hi:[0,0,0] cbsz:1
	s_setprio 0
	s_nop 15
	s_nop 5
	s_nop 0
	v_cvt_pknorm_u16_f32 v50, v50, v51
	v_cvt_pknorm_u16_f32 v51, v52, v53
	v_perm_b32 v102, v51, v50, s86
	v_cvt_pknorm_u16_f32 v50, v70, v71
	v_cvt_pknorm_u16_f32 v51, v72, v73
	v_cvt_pknorm_u16_f32 v66, v66, v67
	v_cvt_pknorm_u16_f32 v67, v68, v69
	v_perm_b32 v99, v51, v50, s86
	v_cvt_pknorm_u16_f32 v50, v54, v55
	v_cvt_pknorm_u16_f32 v51, v56, v57
	v_perm_b32 v98, v67, v66, s86
	v_perm_b32 v103, v51, v50, s86
	s_waitcnt lgkmcnt(0)
	v_mfma_scale_f32_32x32x64_f8f6f4 v[18:33], v[90:97], v[114:121], v[18:33], v145, v145 op_sel_hi:[0,0,0] cbsz:1
	ds_read_b128 v[130:133], v147 offset:4096
	ds_read_b128 v[134:137], v147 offset:4608
	v_cvt_pknorm_u16_f32 v50, v74, v75
	v_cvt_pknorm_u16_f32 v51, v76, v77
	v_perm_b32 v100, v51, v50, s86
	v_cvt_pknorm_u16_f32 v50, v58, v59
	v_cvt_pknorm_u16_f32 v51, v60, v61
	v_perm_b32 v104, v51, v50, s86
	v_cvt_pknorm_u16_f32 v50, v78, v79
	v_cvt_pknorm_u16_f32 v51, v80, v81
	v_perm_b32 v101, v51, v50, s86
	v_cvt_pknorm_u16_f32 v50, v62, v63
	v_cvt_pknorm_u16_f32 v51, v64, v65
	v_perm_b32 v105, v51, v50, s86
	v_mov_b32_e32 v126, v219
	v_mov_b32_e32 v127, v219
	v_mov_b32_e32 v128, v219
	v_mov_b32_e32 v129, v219
	v_mfma_scale_f32_16x16x128_f8f6f4 v[126:129], v[90:97], v[82:89], v[126:129], v145, v145 op_sel_hi:[0,0,0] cbsz:1
	s_mov_b64 s[10:11], -1
	s_and_b64 vcc, exec, s[8:9]
	s_cbranch_vccz .LBB0_731
	s_waitcnt vmcnt(1) lgkmcnt(0)
	s_barrier
	s_cbranch_execz .LBB0_732

.LBB0_724:
	s_lshl_b32 s10, s31, 6
	s_add_u32 s10, s6, s10
	s_addc_u32 s11, s7, 0
	v_lshl_add_u64 v[50:51], s[10:11], 0, v[218:219]
	s_mov_b32 m0, s26
	s_nop 0
	global_load_lds_dwordx4 v[50:51], off
.LBB0_725:
	s_min_i32 s10, s27, -3
	s_sub_i32 s10, s10, s27
	s_ashr_i32 s11, s10, 31
	s_lshl_b64 s[10:11], s[10:11], 6
	s_add_u32 s10, s29, s10
	s_addc_u32 s11, s30, s11
	v_lshl_add_u64 v[50:51], s[10:11], 0, v[140:141]
	s_mov_b64 s[10:11], 0x180
	v_lshl_add_u64 v[50:51], v[50:51], 0, s[10:11]
	s_add_i32 s10, s28, 0x6000
	s_mov_b32 m0, s10
	s_nop 0
	global_load_lds_dwordx4 v[50:51], off
	s_setprio 1
	s_waitcnt lgkmcnt(1)
	v_mfma_scale_f32_32x32x64_f8f6f4 v[50:65], v[130:133], v[122:125], v[2:17], v149, v148 op_sel_hi:[0,0,0] cbsz:4 blgp:4
	s_waitcnt lgkmcnt(0)
	v_mfma_scale_f32_32x32x64_f8f6f4 v[66:81], v[134:137], v[122:125], v[2:17], v149, v148 op_sel_hi:[0,0,0] cbsz:4 blgp:4
	ds_read_b128 v[106:109], v146 offset:20480
	ds_read_b128 v[114:117], v146 offset:20992
	ds_read_b128 v[110:113], v146 offset:21504
	ds_read_b128 v[118:121], v146 offset:22016
	s_waitcnt lgkmcnt(1)
	v_mfma_scale_f32_32x32x64_f8f6f4 v[34:49], v[98:105], v[106:113], v[34:49], v145, v145 op_sel_hi:[0,0,0] cbsz:1
	s_setprio 0
	s_nop 15
	s_nop 5
	s_nop 0
	v_cvt_pknorm_u16_f32 v50, v50, v51
	v_cvt_pknorm_u16_f32 v51, v52, v53
	v_perm_b32 v150, v51, v50, s86
	v_cvt_pknorm_u16_f32 v50, v66, v67
	v_cvt_pknorm_u16_f32 v51, v68, v69
	v_perm_b32 v154, v51, v50, s86
	v_cvt_pknorm_u16_f32 v50, v54, v55
	v_cvt_pknorm_u16_f32 v51, v56, v57
	v_perm_b32 v151, v51, v50, s86
	v_cvt_pknorm_u16_f32 v50, v70, v71
	v_cvt_pknorm_u16_f32 v51, v72, v73
	v_perm_b32 v155, v51, v50, s86
	s_waitcnt lgkmcnt(0)
	v_mfma_scale_f32_32x32x64_f8f6f4 v[18:33], v[98:105], v[114:121], v[18:33], v145, v145 op_sel_hi:[0,0,0] cbsz:1
	ds_read_b128 v[130:133], v147 offset:6144
	ds_read_b128 v[134:137], v147 offset:6656
	v_cvt_pknorm_u16_f32 v50, v58, v59
	v_cvt_pknorm_u16_f32 v51, v60, v61
	v_perm_b32 v152, v51, v50, s86
	v_cvt_pknorm_u16_f32 v50, v74, v75
	v_cvt_pknorm_u16_f32 v51, v76, v77
	v_perm_b32 v156, v51, v50, s86
	v_cvt_pknorm_u16_f32 v50, v62, v63
	v_cvt_pknorm_u16_f32 v51, v64, v65
	v_perm_b32 v153, v51, v50, s86
	v_cvt_pknorm_u16_f32 v50, v78, v79
	v_cvt_pknorm_u16_f32 v51, v80, v81
	v_perm_b32 v157, v51, v50, s86
	v_mfma_scale_f32_16x16x128_f8f6f4 v[126:129], v[98:105], v[82:89], v[126:129], v145, v145 op_sel_hi:[0,0,0] cbsz:1
	s_setprio 1
	s_waitcnt lgkmcnt(1)
	v_mfma_scale_f32_32x32x64_f8f6f4 v[50:65], v[130:133], v[122:125], v[2:17], v149, v148 op_sel_hi:[0,0,0] cbsz:4 blgp:4
	s_waitcnt lgkmcnt(0)
	v_mfma_scale_f32_32x32x64_f8f6f4 v[66:81], v[134:137], v[122:125], v[2:17], v149, v148 op_sel_hi:[0,0,0] cbsz:4 blgp:4
	ds_read_b128 v[90:93], v146 offset:24576
	ds_read_b128 v[106:109], v146 offset:25088
	ds_read_b128 v[94:97], v146 offset:25600
	ds_read_b128 v[110:113], v146 offset:26112
	s_waitcnt lgkmcnt(1)
	v_mfma_scale_f32_32x32x64_f8f6f4 v[34:49], v[150:157], v[90:97], v[34:49], v145, v145 op_sel_hi:[0,0,0] cbsz:1
	s_setprio 0
	s_nop 15
	s_nop 5
	s_nop 0
	v_cvt_pknorm_u16_f32 v50, v50, v51
	v_cvt_pknorm_u16_f32 v51, v52, v53
	v_perm_b32 v98, v51, v50, s86
	v_cvt_pknorm_u16_f32 v50, v66, v67
	v_cvt_pknorm_u16_f32 v51, v68, v69
	v_perm_b32 v102, v51, v50, s86
	v_cvt_pknorm_u16_f32 v50, v54, v55
	v_cvt_pknorm_u16_f32 v51, v56, v57
	v_perm_b32 v99, v51, v50, s86
	v_cvt_pknorm_u16_f32 v50, v70, v71
	v_cvt_pknorm_u16_f32 v51, v72, v73
	v_perm_b32 v103, v51, v50, s86
	s_waitcnt lgkmcnt(0)
	v_mfma_scale_f32_32x32x64_f8f6f4 v[18:33], v[150:157], v[106:113], v[18:33], v145, v145 op_sel_hi:[0,0,0] cbsz:1
	v_cvt_pknorm_u16_f32 v50, v58, v59
	v_cvt_pknorm_u16_f32 v51, v60, v61
	v_perm_b32 v100, v51, v50, s86
	v_cvt_pknorm_u16_f32 v50, v74, v75
	v_cvt_pknorm_u16_f32 v51, v76, v77
	v_perm_b32 v104, v51, v50, s86
	v_cvt_pknorm_u16_f32 v50, v62, v63
	v_cvt_pknorm_u16_f32 v51, v64, v65
	v_perm_b32 v101, v51, v50, s86
	v_cvt_pknorm_u16_f32 v50, v78, v79
	v_cvt_pknorm_u16_f32 v51, v80, v81
	v_perm_b32 v105, v51, v50, s86
	v_mfma_scale_f32_16x16x128_f8f6f4 v[126:129], v[150:157], v[82:89], v[126:129], v145, v145 op_sel_hi:[0,0,0] cbsz:1
	s_mov_b64 s[10:11], -1
	s_and_b64 vcc, exec, s[8:9]
	s_cbranch_vccz .LBB0_733
	s_waitcnt vmcnt(1) lgkmcnt(0)
	s_barrier
	s_cbranch_execz .LBB0_734

.LBB0_728:
	s_lshl_b32 s4, s31, 6
	s_add_u32 s4, s6, s4
	s_addc_u32 s5, s7, 0
	v_lshl_add_u64 v[50:51], s[4:5], 0, v[218:219]
	s_add_i32 s4, s26, 0x1000
	s_mov_b32 m0, s4
	s_nop 0
	global_load_lds_dwordx4 v[50:51], off
.LBB0_729:
	s_min_i32 s4, s27, -5
	s_sub_i32 s4, s4, s27
	s_ashr_i32 s5, s4, 31
	s_lshl_b64 s[4:5], s[4:5], 6
	s_add_u32 s4, s29, s4
	s_addc_u32 s5, s30, s5
	v_lshl_add_u64 v[50:51], s[4:5], 0, v[140:141]
	s_mov_b64 s[4:5], 0x200
	v_lshl_add_u64 v[50:51], v[50:51], 0, s[4:5]
	s_mov_b32 m0, s28
	s_nop 0
	global_load_lds_dwordx4 v[50:51], off
	ds_read_b128 v[50:53], v146 offset:28672
	ds_read_b128 v[58:61], v146 offset:29184
	ds_read_b128 v[54:57], v146 offset:29696
	ds_read_b128 v[62:65], v146 offset:30208
	s_waitcnt lgkmcnt(1)
	v_mfma_scale_f32_32x32x64_f8f6f4 v[34:49], v[98:105], v[50:57], v[34:49], v145, v145 op_sel_hi:[0,0,0] cbsz:1
	s_waitcnt lgkmcnt(0)
	v_mfma_scale_f32_32x32x64_f8f6f4 v[18:33], v[98:105], v[58:65], v[18:33], v145, v145 op_sel_hi:[0,0,0] cbsz:1
	v_mfma_scale_f32_16x16x128_f8f6f4 v[126:129], v[98:105], v[82:89], v[126:129], v145, v145 op_sel_hi:[0,0,0] cbsz:1
	s_lshl_b32 s3, s3, 11
	s_nop 15
	s_nop 15
	s_waitcnt vmcnt(0) lgkmcnt(0)
	s_barrier
	v_and_b32_e32 v50, 7, v142
	s_add_i32 s3, s17, s3
	v_cmp_eq_u32_e32 vcc, 0, v50
	s_and_saveexec_b64 s[4:5], vcc
	s_cbranch_execz .LBB0_708
	v_lshlrev_b32_e32 v50, 3, v142
	v_and_b32_e32 v50, 64, v50
	v_and_b32_e32 v51, 48, v142
	v_add3_u32 v50, s3, v50, v51
	ds_write_b128 v50, v[126:129]
	s_branch .LBB0_708

.LBB0_738:
	s_lshl_b32 s7, s26, 8
	s_ashr_i32 s6, s26, 7
	s_and_b32 s7, s7, 0xf00
	s_bfe_u32 s10, s26, 0x30004
	s_mul_i32 s4, s6, 0x2100
	s_addk_i32 s7, 0x100
	s_mul_hi_i32 s5, s6, 0x2100
	s_add_u32 s4, s4, s7
	s_addc_u32 s5, s5, 0
	s_lshl_b64 s[4:5], s[4:5], 9
	s_add_u32 s8, s18, s4
	s_addc_u32 s9, s19, s5
	s_lshl_b32 s7, s10, 6
	s_add_u32 s12, s8, s7
	s_addc_u32 s13, s9, 0
	s_mul_i32 s9, s6, 0x420000
	s_mul_hi_i32 s8, s6, 0x420000
	s_add_u32 s9, s20, s9
	s_addc_u32 s11, s21, s8
	s_add_u32 s8, s9, s7
	s_addc_u32 s9, s11, 0
	s_lshl_b32 s6, s6, 3
	s_or_b32 s6, s6, s10
	s_mul_hi_i32 s11, s6, 0x84000
	s_mul_i32 s6, s6, 0x84000
	v_mov_b32_e32 v217, v0
	s_add_u32 s10, s22, s6
	s_addc_u32 s11, s23, s11
	v_readfirstlane_b32 s6, v217
	s_ashr_i32 s28, s6, 8
	s_ashr_i32 s27, s6, 6
	s_lshl_b32 s6, s28, 12
	v_and_b32_e32 v225, 31, v217
	s_add_i32 s31, s6, s15
	s_lshl_b32 s6, s27, 5
	v_or_b32_e32 v18, s6, v225
	v_ashrrev_i32_e32 v19, 31, v18
	v_bfe_u32 v226, v217, 5, 1
	v_lshlrev_b64 v[18:19], 9, v[18:19]
	v_lshl_add_u64 v[18:19], s[12:13], 0, v[18:19]
	v_lshlrev_b32_e32 v210, 4, v226
	v_mov_b32_e32 v211, v219
	v_lshl_add_u64 v[18:19], v[18:19], 0, v[210:211]
	s_mov_b32 s12, 0x200000
	global_load_dwordx4 v[170:173], v[18:19], off
	s_waitcnt vmcnt(0)
	global_load_dwordx4 v[174:177], v[18:19], off offset:32
	v_add_co_u32_e32 v18, vcc, s12, v18
	s_waitcnt vmcnt(0)
	s_lshl_b32 s30, s28, 6
	v_addc_co_u32_e32 v19, vcc, 0, v19, vcc
	global_load_dwordx4 v[178:181], v[18:19], off
	s_waitcnt vmcnt(0)
	global_load_dwordx4 v[182:185], v[18:19], off offset:32
	v_and_b32_e32 v224, 63, v217
	v_mov_b32_e32 v18, s30
	s_movk_i32 s12, 0x2100
	s_and_b32 s29, s27, 3
	v_mad_u32_u24 v18, v224, s12, v18
	s_min_i32 s12, s28, 0x83
	s_lshl_b32 s33, s29, 4
	s_lshl_b32 s29, s29, 10
	s_sub_i32 s12, s12, s28
	s_add_i32 s29, s29, s31
	s_ashr_i32 s13, s12, 31
	s_add_i32 s31, s29, 0x8000
	s_lshl_b64 s[34:35], s[12:13], 6
	s_lshl_b64 s[12:13], s[12:13], 15
	v_or_b32_e32 v20, s30, v224
	s_add_u32 s12, s8, s12
	v_lshl_or_b32 v218, v20, 9, s33
	s_addc_u32 s13, s9, s13
	s_waitcnt vmcnt(0)
	v_or_b32_e32 v212, s33, v18
	v_lshl_add_u64 v[18:19], s[12:13], 0, v[218:219]
	s_mov_b32 m0, s29
	s_nop 0
	global_load_lds_dwordx4 v[18:19], off
	s_min_i32 s12, s28, 0x81
	s_sub_i32 s12, s12, s28
	s_add_i32 s12, s12, 2
	s_ashr_i32 s13, s12, 31
	s_lshl_b64 s[38:39], s[12:13], 6
	s_lshl_b64 s[12:13], s[12:13], 15
	s_add_u32 s12, s8, s12
	s_addc_u32 s13, s9, s13
	v_lshl_add_u64 v[18:19], s[12:13], 0, v[218:219]
	s_add_i32 s12, s29, 0x2000
	s_mov_b32 m0, s12
	s_nop 0
	global_load_lds_dwordx4 v[18:19], off
	s_add_u32 s12, s10, s34
	v_mov_b32_e32 v213, v219
	s_addc_u32 s13, s11, s35
	v_lshl_add_u64 v[18:19], s[12:13], 0, v[212:213]
	s_mov_b32 m0, s31
	s_nop 0
	global_load_lds_dwordx4 v[18:19], off
	s_min_i32 s12, s28, 0x7f
	s_sub_i32 s12, s12, s28
	s_add_i32 s34, s12, 4
	s_ashr_i32 s35, s34, 31
	s_lshl_b64 s[12:13], s[34:35], 15
	s_add_u32 s12, s8, s12
	s_addc_u32 s13, s9, s13
	v_lshl_add_u64 v[18:19], s[12:13], 0, v[218:219]
	s_add_i32 s12, s29, 0x4000
	s_mov_b32 m0, s12
	s_nop 0
	global_load_lds_dwordx4 v[18:19], off
	s_add_u32 s12, s10, s38
	s_addc_u32 s13, s11, s39
	v_lshl_add_u64 v[18:19], s[12:13], 0, v[212:213]
	s_add_i32 s12, s31, 0x2000
	s_mov_b32 m0, s12
	s_nop 0
	global_load_lds_dwordx4 v[18:19], off
	s_min_i32 s12, s28, 0x7d
	s_sub_i32 s12, s12, s28
	s_add_i32 s38, s12, 6
	s_ashr_i32 s39, s38, 31
	s_lshl_b64 s[12:13], s[38:39], 6
	s_lshl_b64 s[38:39], s[38:39], 15
	v_lshlrev_b32_e32 v21, 10, v226
	v_lshlrev_b32_e32 v66, 4, v225
	s_add_u32 s38, s8, s38
	v_add3_u32 v211, s15, v21, v66
	v_lshrrev_b32_e32 v18, 4, v217
	v_lshrrev_b32_e32 v19, 3, v217
	s_waitcnt vmcnt(2) lgkmcnt(0)
	s_barrier
	s_addc_u32 s39, s9, s39
	s_add_i32 s33, s29, 0x6000
	s_lshl_b64 s[34:35], s[34:35], 6
	v_bitop3_b32 v18, v18, 1, v19 bitop3:0x48
	ds_read_b128 v[50:53], v211
	ds_read_b128 v[58:61], v211 offset:2048
	ds_read_b128 v[54:57], v211 offset:512
	ds_read_b128 v[62:65], v211 offset:2560
	s_waitcnt lgkmcnt(0)
	s_barrier
	s_add_u32 s34, s10, s34
	v_cmp_eq_u32_e32 vcc, 0, v18
	v_lshl_add_u64 v[18:19], s[38:39], 0, v[218:219]
	s_mov_b32 m0, s33
	s_nop 0
	global_load_lds_dwordx4 v[18:19], off
	s_addc_u32 s35, s11, s35
	v_lshl_add_u64 v[18:19], s[34:35], 0, v[212:213]
	s_add_i32 s33, s31, 0x4000
	s_mov_b32 m0, s33
	s_nop 0
	global_load_lds_dwordx4 v[18:19], off
	v_cndmask_b32_e32 v114, 0, v237, vcc
	v_mov_b32_e32 v227, 0x7f7f7f7f
	v_mov_b32_e32 v228, 0x76767676
	v_mov_b32_e32 v229, 0x7e7e7e7e
	v_lshlrev_b32_e32 v67, 11, v226
	s_mov_b32 s30, 0x8000
	v_mov_b32_e32 v115, v114
	v_mov_b32_e32 v116, v114
	v_mov_b32_e32 v117, v114
	v_mov_b32_e32 v118, v114
	v_mov_b32_e32 v119, v114
	v_mov_b32_e32 v120, v114
	v_mov_b32_e32 v121, v114
	s_waitcnt lgkmcnt(3)
	v_mfma_scale_f32_32x32x64_f8f6f4 v[34:49], v[50:53], v[170:173], v[2:17], v229, v228 op_sel_hi:[0,0,0] cbsz:4 blgp:4
	s_waitcnt lgkmcnt(1)
	v_mfma_scale_f32_32x32x64_f8f6f4 v[18:33], v[54:57], v[170:173], v[2:17], v229, v228 op_sel_hi:[0,0,0] cbsz:4 blgp:4
	v_mfma_scale_f32_32x32x64_f8f6f4 v[34:49], v[58:61], v[174:177], v[34:49], v229, v228 op_sel_hi:[0,0,0] cbsz:4 blgp:4
	s_waitcnt lgkmcnt(0)
	v_mfma_scale_f32_32x32x64_f8f6f4 v[18:33], v[62:65], v[174:177], v[18:33], v229, v228 op_sel_hi:[0,0,0] cbsz:4 blgp:4
	s_nop 0
	s_nop 15
	s_nop 15
	s_nop 0
	v_cvt_pknorm_u16_f32 v18, v18, v19
	v_cvt_pknorm_u16_f32 v19, v20, v21
	v_perm_b32 v126, v19, v18, s86
	v_cvt_pknorm_u16_f32 v18, v38, v39
	v_cvt_pknorm_u16_f32 v19, v40, v41
	v_perm_b32 v123, v19, v18, s86
	v_cvt_pknorm_u16_f32 v18, v22, v23
	v_cvt_pknorm_u16_f32 v19, v24, v25
	v_perm_b32 v127, v19, v18, s86
	v_cvt_pknorm_u16_f32 v18, v42, v43
	v_cvt_pknorm_u16_f32 v19, v44, v45
	v_perm_b32 v124, v19, v18, s86
	v_cvt_pknorm_u16_f32 v18, v26, v27
	v_cvt_pknorm_u16_f32 v19, v28, v29
	v_perm_b32 v128, v19, v18, s86
	v_cvt_pknorm_u16_f32 v18, v46, v47
	v_cvt_pknorm_u16_f32 v19, v48, v49
	v_cvt_pknorm_u16_f32 v34, v34, v35
	v_cvt_pknorm_u16_f32 v35, v36, v37
	v_perm_b32 v125, v19, v18, s86
	v_cvt_pknorm_u16_f32 v18, v30, v31
	v_cvt_pknorm_u16_f32 v19, v32, v33
	v_perm_b32 v122, v35, v34, s86
	v_perm_b32 v129, v19, v18, s86
	v_mfma_scale_f32_32x32x64_f8f6f4 v[34:49], v[50:53], v[178:181], v[2:17], v229, v228 op_sel_hi:[0,0,0] cbsz:4 blgp:4
	v_mfma_scale_f32_32x32x64_f8f6f4 v[18:33], v[54:57], v[178:181], v[2:17], v229, v228 op_sel_hi:[0,0,0] cbsz:4 blgp:4
	s_nop 0
	v_mfma_scale_f32_32x32x64_f8f6f4 v[34:49], v[58:61], v[182:185], v[34:49], v229, v228 op_sel_hi:[0,0,0] cbsz:4 blgp:4
	v_mfma_scale_f32_32x32x64_f8f6f4 v[18:33], v[62:65], v[182:185], v[18:33], v229, v228 op_sel_hi:[0,0,0] cbsz:4 blgp:4
	s_nop 0
	s_nop 15
	s_nop 15
	s_nop 0
	v_cvt_pknorm_u16_f32 v18, v18, v19
	v_cvt_pknorm_u16_f32 v19, v20, v21
	v_perm_b32 v134, v19, v18, s86
	v_cvt_pknorm_u16_f32 v18, v38, v39
	v_cvt_pknorm_u16_f32 v19, v40, v41
	v_perm_b32 v131, v19, v18, s86
	v_cvt_pknorm_u16_f32 v18, v22, v23
	v_cvt_pknorm_u16_f32 v19, v24, v25
	v_perm_b32 v135, v19, v18, s86
	v_cvt_pknorm_u16_f32 v18, v42, v43
	v_cvt_pknorm_u16_f32 v19, v44, v45
	v_perm_b32 v132, v19, v18, s86
	v_cvt_pknorm_u16_f32 v18, v26, v27
	v_cvt_pknorm_u16_f32 v19, v28, v29
	v_perm_b32 v136, v19, v18, s86
	v_cvt_pknorm_u16_f32 v18, v46, v47
	v_cvt_pknorm_u16_f32 v19, v48, v49
	v_cvt_pknorm_u16_f32 v34, v34, v35
	v_cvt_pknorm_u16_f32 v35, v36, v37
	v_perm_b32 v133, v19, v18, s86
	v_cvt_pknorm_u16_f32 v18, v30, v31
	v_cvt_pknorm_u16_f32 v19, v32, v33
	v_perm_b32 v130, v35, v34, s86
	v_perm_b32 v137, v19, v18, s86
	ds_read_b128 v[194:197], v211 offset:4096
	ds_read_b128 v[198:201], v211 offset:4608
	ds_read_b128 v[202:205], v211 offset:6144
	ds_read_b128 v[206:209], v211 offset:6656
	v_add3_u32 v244, s15, v67, v66
	s_setprio 1
	s_waitcnt lgkmcnt(3)
	v_mfma_scale_f32_32x32x64_f8f6f4 v[74:89], v[194:197], v[170:173], v[2:17], v229, v228 op_sel_hi:[0,0,0] cbsz:4 blgp:4
	s_waitcnt lgkmcnt(2)
	v_mfma_scale_f32_32x32x64_f8f6f4 v[34:49], v[198:201], v[170:173], v[2:17], v229, v228 op_sel_hi:[0,0,0] cbsz:4 blgp:4
	s_waitcnt lgkmcnt(1)
	v_mfma_scale_f32_32x32x64_f8f6f4 v[74:89], v[202:205], v[174:177], v[74:89], v229, v228 op_sel_hi:[0,0,0] cbsz:4 blgp:4
	s_waitcnt lgkmcnt(0)
	v_mfma_scale_f32_32x32x64_f8f6f4 v[34:49], v[206:209], v[174:177], v[34:49], v229, v228 op_sel_hi:[0,0,0] cbsz:4 blgp:4
	ds_read_b128 v[154:157], v244 offset:32768
	ds_read_b128 v[162:165], v244 offset:33280
	ds_read_b128 v[158:161], v244 offset:33792
	ds_read_b128 v[166:169], v244 offset:34304
	v_readlane_b32 s40, v255, 8
	v_readlane_b32 s41, v255, 9
	v_readlane_b32 s42, v255, 10
	v_readlane_b32 s43, v255, 11
	v_readlane_b32 s44, v255, 12
	v_readlane_b32 s45, v255, 13
	v_readlane_b32 s46, v255, 14
	v_readlane_b32 s47, v255, 15
	v_readlane_b32 s48, v255, 16
	v_readlane_b32 s49, v255, 17
	v_readlane_b32 s50, v255, 18
	v_readlane_b32 s51, v255, 19
	v_readlane_b32 s52, v255, 20
	v_readlane_b32 s53, v255, 21
	v_readlane_b32 s54, v255, 22
	v_readlane_b32 s55, v255, 23
	v_mov_b64_e32 v[18:19], s[40:41]
	v_mov_b64_e32 v[20:21], s[42:43]
	v_mov_b64_e32 v[32:33], s[54:55]
	v_mov_b64_e32 v[22:23], s[44:45]
	v_mov_b64_e32 v[24:25], s[46:47]
	v_mov_b64_e32 v[26:27], s[48:49]
	v_mov_b64_e32 v[28:29], s[50:51]
	v_mov_b64_e32 v[30:31], s[52:53]
	v_mov_b64_e32 v[64:65], v[32:33]
	v_mov_b64_e32 v[62:63], v[30:31]
	v_mov_b64_e32 v[60:61], v[28:29]
	v_mov_b64_e32 v[58:59], v[26:27]
	v_mov_b64_e32 v[56:57], v[24:25]
	v_mov_b64_e32 v[54:55], v[22:23]
	v_mov_b64_e32 v[52:53], v[20:21]
	v_mov_b64_e32 v[50:51], v[18:19]
	s_waitcnt lgkmcnt(1)
	v_mfma_scale_f32_32x32x64_f8f6f4 v[50:65], v[122:129], v[154:161], v[50:65], v227, v227 op_sel_hi:[0,0,0] cbsz:1
	s_setprio 0
	s_nop 15
	s_nop 15
	s_nop 0
	v_cvt_pknorm_u16_f32 v34, v34, v35
	v_cvt_pknorm_u16_f32 v35, v36, v37
	v_perm_b32 v142, v35, v34, s86
	v_cvt_pknorm_u16_f32 v34, v78, v79
	v_cvt_pknorm_u16_f32 v35, v80, v81
	v_cvt_pknorm_u16_f32 v66, v74, v75
	v_cvt_pknorm_u16_f32 v67, v76, v77
	v_perm_b32 v139, v35, v34, s86
	v_cvt_pknorm_u16_f32 v34, v38, v39
	v_cvt_pknorm_u16_f32 v35, v40, v41
	v_perm_b32 v138, v67, v66, s86
	v_perm_b32 v143, v35, v34, s86
	v_mov_b64_e32 v[80:81], v[32:33]
	v_mov_b64_e32 v[78:79], v[30:31]
	v_mov_b64_e32 v[76:77], v[28:29]
	v_mov_b64_e32 v[74:75], v[26:27]
	v_mov_b64_e32 v[72:73], v[24:25]
	v_mov_b64_e32 v[70:71], v[22:23]
	v_mov_b64_e32 v[68:69], v[20:21]
	v_mov_b64_e32 v[66:67], v[18:19]
	s_waitcnt lgkmcnt(0)
	v_mfma_scale_f32_32x32x64_f8f6f4 v[66:81], v[122:129], v[162:169], v[66:81], v227, v227 op_sel_hi:[0,0,0] cbsz:1
	v_cvt_pknorm_u16_f32 v34, v82, v83
	v_cvt_pknorm_u16_f32 v35, v84, v85
	v_perm_b32 v140, v35, v34, s86
	v_cvt_pknorm_u16_f32 v34, v42, v43
	v_cvt_pknorm_u16_f32 v35, v44, v45
	v_perm_b32 v144, v35, v34, s86
	v_cvt_pknorm_u16_f32 v34, v86, v87
	v_cvt_pknorm_u16_f32 v35, v88, v89
	v_perm_b32 v141, v35, v34, s86
	v_cvt_pknorm_u16_f32 v34, v46, v47
	v_cvt_pknorm_u16_f32 v35, v48, v49
	v_perm_b32 v145, v35, v34, s86
	v_mov_b64_e32 v[188:189], s[90:91]
	v_mov_b64_e32 v[192:193], s[90:91]
	v_mov_b64_e32 v[186:187], s[88:89]
	v_mov_b64_e32 v[190:191], s[88:89]
	v_mfma_scale_f32_16x16x128_f8f6f4 v[190:193], v[122:129], v[114:121], v[190:193], v227, v227 op_sel_hi:[0,0,0] cbsz:1
	s_setprio 1
	v_mfma_scale_f32_32x32x64_f8f6f4 v[98:113], v[194:197], v[178:181], v[2:17], v229, v228 op_sel_hi:[0,0,0] cbsz:4 blgp:4
	v_mfma_scale_f32_32x32x64_f8f6f4 v[82:97], v[198:201], v[178:181], v[2:17], v229, v228 op_sel_hi:[0,0,0] cbsz:4 blgp:4
	s_nop 0
	v_mfma_scale_f32_32x32x64_f8f6f4 v[98:113], v[202:205], v[182:185], v[98:113], v229, v228 op_sel_hi:[0,0,0] cbsz:4 blgp:4
	v_mfma_scale_f32_32x32x64_f8f6f4 v[82:97], v[206:209], v[182:185], v[82:97], v229, v228 op_sel_hi:[0,0,0] cbsz:4 blgp:4
	v_mov_b64_e32 v[48:49], v[32:33]
	v_mov_b64_e32 v[46:47], v[30:31]
	v_mov_b64_e32 v[44:45], v[28:29]
	v_mov_b64_e32 v[42:43], v[26:27]
	v_mov_b64_e32 v[40:41], v[24:25]
	v_mov_b64_e32 v[38:39], v[22:23]
	v_mov_b64_e32 v[36:37], v[20:21]
	v_mov_b64_e32 v[34:35], v[18:19]
	v_mfma_scale_f32_32x32x64_f8f6f4 v[34:49], v[130:137], v[154:161], v[34:49], v227, v227 op_sel_hi:[0,0,0] cbsz:1
	s_setprio 0
	s_nop 15
	s_nop 15
	s_nop 0
	v_cvt_pknorm_u16_f32 v82, v82, v83
	v_cvt_pknorm_u16_f32 v83, v84, v85
	v_perm_b32 v150, v83, v82, s86
	v_cvt_pknorm_u16_f32 v82, v102, v103
	v_cvt_pknorm_u16_f32 v83, v104, v105
	v_cvt_pknorm_u16_f32 v98, v98, v99
	v_cvt_pknorm_u16_f32 v99, v100, v101
	v_perm_b32 v147, v83, v82, s86
	v_cvt_pknorm_u16_f32 v82, v86, v87
	v_cvt_pknorm_u16_f32 v83, v88, v89
	v_perm_b32 v146, v99, v98, s86
	v_perm_b32 v151, v83, v82, s86
	v_mfma_scale_f32_32x32x64_f8f6f4 v[18:33], v[130:137], v[162:169], v[18:33], v227, v227 op_sel_hi:[0,0,0] cbsz:1
	ds_read_b128 v[194:197], v211 offset:8192
	ds_read_b128 v[198:201], v211 offset:8704
	ds_read_b128 v[206:209], v211 offset:10240
	ds_read_b128 v[202:205], v211 offset:10752
	v_cvt_pknorm_u16_f32 v82, v106, v107
	v_cvt_pknorm_u16_f32 v83, v108, v109
	v_perm_b32 v148, v83, v82, s86
	v_cvt_pknorm_u16_f32 v82, v90, v91
	v_cvt_pknorm_u16_f32 v83, v92, v93
	v_perm_b32 v152, v83, v82, s86
	v_cvt_pknorm_u16_f32 v82, v110, v111
	v_cvt_pknorm_u16_f32 v83, v112, v113
	v_perm_b32 v149, v83, v82, s86
	v_cvt_pknorm_u16_f32 v82, v94, v95
	v_cvt_pknorm_u16_f32 v83, v96, v97
	v_perm_b32 v153, v83, v82, s86
	v_mfma_scale_f32_16x16x128_f8f6f4 v[186:189], v[130:137], v[114:121], v[186:189], v227, v227 op_sel_hi:[0,0,0] cbsz:1
	s_min_i32 s33, s28, 0x7b
	s_sub_i32 s34, s33, s28
	s_ashr_i32 s35, s34, 31
	s_lshl_b64 s[34:35], s[34:35], 15
	s_add_u32 s34, s8, s34
	s_addc_u32 s35, s9, s35
	s_waitcnt vmcnt(2) lgkmcnt(0)
	s_barrier
	v_lshl_add_u64 v[82:83], s[34:35], 0, v[218:219]
	s_mov_b64 s[34:35], 0x40000
	s_add_u32 s12, s10, s12
	v_lshl_add_u64 v[82:83], v[82:83], 0, s[34:35]
	s_mov_b32 m0, s29
	s_nop 0
	global_load_lds_dwordx4 v[82:83], off
	s_addc_u32 s13, s11, s13
	v_lshl_add_u64 v[82:83], s[12:13], 0, v[212:213]
	s_add_i32 s12, s31, 0x6000
	s_mov_b32 m0, s12
	s_nop 0
	global_load_lds_dwordx4 v[82:83], off
	v_lshl_add_u64 v[214:215], s[8:9], 0, v[218:219]
	v_lshl_add_u64 v[212:213], s[10:11], 0, v[212:213]
	s_add_i32 s8, s28, 10
.LBB0_739:
	s_setprio 1
	s_waitcnt lgkmcnt(3)
	v_mfma_scale_f32_32x32x64_f8f6f4 v[82:97], v[194:197], v[170:173], v[2:17], v229, v228 op_sel_hi:[0,0,0] cbsz:4 blgp:4
	s_waitcnt lgkmcnt(2)
	v_mfma_scale_f32_32x32x64_f8f6f4 v[98:113], v[198:201], v[170:173], v[2:17], v229, v228 op_sel_hi:[0,0,0] cbsz:4 blgp:4
	s_waitcnt lgkmcnt(1)
	v_mfma_scale_f32_32x32x64_f8f6f4 v[82:97], v[206:209], v[174:177], v[82:97], v229, v228 op_sel_hi:[0,0,0] cbsz:4 blgp:4
	s_waitcnt lgkmcnt(0)
	v_mfma_scale_f32_32x32x64_f8f6f4 v[98:113], v[202:205], v[174:177], v[98:113], v229, v228 op_sel_hi:[0,0,0] cbsz:4 blgp:4
	s_and_b32 s9, s30, 0x6000
	v_add_u32_e32 v166, s9, v244
	ds_read_b128 v[154:157], v166 offset:36864
	ds_read_b128 v[162:165], v166 offset:37376
	ds_read_b128 v[158:161], v166 offset:37888
	ds_read_b128 v[166:169], v166 offset:38400
	s_add_i32 s10, s30, 0xffffa000
	s_waitcnt lgkmcnt(1)
	v_mfma_scale_f32_32x32x64_f8f6f4 v[50:65], v[138:145], v[154:161], v[50:65], v227, v227 op_sel_hi:[0,0,0] cbsz:1
	s_setprio 0
	s_nop 15
	s_nop 15
	s_nop 0
	v_cvt_pknorm_u16_f32 v82, v82, v83
	v_cvt_pknorm_u16_f32 v83, v84, v85
	v_perm_b32 v122, v83, v82, s86
	v_cvt_pknorm_u16_f32 v82, v98, v99
	v_cvt_pknorm_u16_f32 v83, v100, v101
	v_perm_b32 v126, v83, v82, s86
	v_cvt_pknorm_u16_f32 v82, v86, v87
	v_cvt_pknorm_u16_f32 v83, v88, v89
	v_perm_b32 v123, v83, v82, s86
	v_cvt_pknorm_u16_f32 v82, v102, v103
	v_cvt_pknorm_u16_f32 v83, v104, v105
	v_perm_b32 v127, v83, v82, s86
	s_waitcnt lgkmcnt(0)
	v_mfma_scale_f32_32x32x64_f8f6f4 v[66:81], v[138:145], v[162:169], v[66:81], v227, v227 op_sel_hi:[0,0,0] cbsz:1
	v_cvt_pknorm_u16_f32 v82, v90, v91
	v_cvt_pknorm_u16_f32 v83, v92, v93
	v_perm_b32 v124, v83, v82, s86
	v_cvt_pknorm_u16_f32 v82, v106, v107
	v_cvt_pknorm_u16_f32 v83, v108, v109
	v_perm_b32 v128, v83, v82, s86
	v_cvt_pknorm_u16_f32 v82, v94, v95
	v_cvt_pknorm_u16_f32 v83, v96, v97
	v_perm_b32 v125, v83, v82, s86
	v_cvt_pknorm_u16_f32 v82, v110, v111
	v_cvt_pknorm_u16_f32 v83, v112, v113
	v_perm_b32 v129, v83, v82, s86
	v_mfma_scale_f32_16x16x128_f8f6f4 v[190:193], v[138:145], v[114:121], v[190:193], v227, v227 op_sel_hi:[0,0,0] cbsz:1
	s_setprio 1
	v_mfma_scale_f32_32x32x64_f8f6f4 v[82:97], v[194:197], v[178:181], v[2:17], v229, v228 op_sel_hi:[0,0,0] cbsz:4 blgp:4
	v_mfma_scale_f32_32x32x64_f8f6f4 v[98:113], v[198:201], v[178:181], v[2:17], v229, v228 op_sel_hi:[0,0,0] cbsz:4 blgp:4
	s_nop 0
	v_mfma_scale_f32_32x32x64_f8f6f4 v[82:97], v[206:209], v[182:185], v[82:97], v229, v228 op_sel_hi:[0,0,0] cbsz:4 blgp:4
	v_mfma_scale_f32_32x32x64_f8f6f4 v[98:113], v[202:205], v[182:185], v[98:113], v229, v228 op_sel_hi:[0,0,0] cbsz:4 blgp:4
	v_mfma_scale_f32_32x32x64_f8f6f4 v[34:49], v[146:153], v[154:161], v[34:49], v227, v227 op_sel_hi:[0,0,0] cbsz:1
	s_setprio 0
	s_nop 15
	s_nop 15
	s_nop 0
	v_cvt_pknorm_u16_f32 v82, v82, v83
	v_cvt_pknorm_u16_f32 v83, v84, v85
	v_perm_b32 v130, v83, v82, s86
	v_cvt_pknorm_u16_f32 v82, v98, v99
	v_cvt_pknorm_u16_f32 v83, v100, v101
	v_perm_b32 v134, v83, v82, s86
	v_cvt_pknorm_u16_f32 v82, v86, v87
	v_cvt_pknorm_u16_f32 v83, v88, v89
	v_perm_b32 v131, v83, v82, s86
	v_cvt_pknorm_u16_f32 v82, v102, v103
	v_cvt_pknorm_u16_f32 v83, v104, v105
	v_perm_b32 v135, v83, v82, s86
	v_mfma_scale_f32_32x32x64_f8f6f4 v[18:33], v[146:153], v[162:169], v[18:33], v227, v227 op_sel_hi:[0,0,0] cbsz:1
	s_and_b32 s10, s10, 0x6000
	v_add_u32_e32 v82, s10, v211
	ds_read_b128 v[194:197], v82 offset:4096
	ds_read_b128 v[198:201], v82 offset:4608
	ds_read_b128 v[202:205], v82 offset:6144
	ds_read_b128 v[206:209], v82 offset:6656
	v_cvt_pknorm_u16_f32 v82, v90, v91
	v_cvt_pknorm_u16_f32 v83, v92, v93
	v_perm_b32 v132, v83, v82, s86
	v_cvt_pknorm_u16_f32 v82, v106, v107
	v_cvt_pknorm_u16_f32 v83, v108, v109
	v_perm_b32 v136, v83, v82, s86
	v_cvt_pknorm_u16_f32 v82, v94, v95
	v_cvt_pknorm_u16_f32 v83, v96, v97
	v_perm_b32 v133, v83, v82, s86
	v_cvt_pknorm_u16_f32 v82, v110, v111
	v_cvt_pknorm_u16_f32 v83, v112, v113
	v_perm_b32 v137, v83, v82, s86
	v_mfma_scale_f32_16x16x128_f8f6f4 v[186:189], v[146:153], v[114:121], v[186:189], v227, v227 op_sel_hi:[0,0,0] cbsz:1
	s_setprio 1
	s_waitcnt lgkmcnt(3)
	v_mfma_scale_f32_32x32x64_f8f6f4 v[82:97], v[194:197], v[170:173], v[2:17], v229, v228 op_sel_hi:[0,0,0] cbsz:4 blgp:4
	s_waitcnt lgkmcnt(2)
	v_mfma_scale_f32_32x32x64_f8f6f4 v[98:113], v[198:201], v[170:173], v[2:17], v229, v228 op_sel_hi:[0,0,0] cbsz:4 blgp:4
	s_waitcnt lgkmcnt(1)
	v_mfma_scale_f32_32x32x64_f8f6f4 v[82:97], v[202:205], v[174:177], v[82:97], v229, v228 op_sel_hi:[0,0,0] cbsz:4 blgp:4
	s_waitcnt lgkmcnt(0)
	v_mfma_scale_f32_32x32x64_f8f6f4 v[98:113], v[206:209], v[174:177], v[98:113], v229, v228 op_sel_hi:[0,0,0] cbsz:4 blgp:4
	v_add_u32_e32 v166, s10, v244
	ds_read_b128 v[154:157], v166 offset:32768
	ds_read_b128 v[162:165], v166 offset:33280
	ds_read_b128 v[158:161], v166 offset:33792
	ds_read_b128 v[166:169], v166 offset:34304
	s_waitcnt lgkmcnt(1)
	v_mfma_scale_f32_32x32x64_f8f6f4 v[50:65], v[122:129], v[154:161], v[50:65], v227, v227 op_sel_hi:[0,0,0] cbsz:1
	s_setprio 0
	s_nop 15
	s_nop 15
	s_nop 0
	v_cvt_pknorm_u16_f32 v82, v82, v83
	v_cvt_pknorm_u16_f32 v83, v84, v85
	v_perm_b32 v138, v83, v82, s86
	v_cvt_pknorm_u16_f32 v82, v98, v99
	v_cvt_pknorm_u16_f32 v83, v100, v101
	v_perm_b32 v142, v83, v82, s86
	v_cvt_pknorm_u16_f32 v82, v86, v87
	v_cvt_pknorm_u16_f32 v83, v88, v89
	v_perm_b32 v139, v83, v82, s86
	v_cvt_pknorm_u16_f32 v82, v102, v103
	v_cvt_pknorm_u16_f32 v83, v104, v105
	v_perm_b32 v143, v83, v82, s86
	s_waitcnt lgkmcnt(0)
	v_mfma_scale_f32_32x32x64_f8f6f4 v[66:81], v[122:129], v[162:169], v[66:81], v227, v227 op_sel_hi:[0,0,0] cbsz:1
	v_cvt_pknorm_u16_f32 v82, v90, v91
	v_cvt_pknorm_u16_f32 v83, v92, v93
	v_perm_b32 v140, v83, v82, s86
	v_cvt_pknorm_u16_f32 v82, v106, v107
	v_cvt_pknorm_u16_f32 v83, v108, v109
	v_perm_b32 v144, v83, v82, s86
	v_cvt_pknorm_u16_f32 v82, v94, v95
	v_cvt_pknorm_u16_f32 v83, v96, v97
	v_perm_b32 v141, v83, v82, s86
	v_cvt_pknorm_u16_f32 v82, v110, v111
	v_cvt_pknorm_u16_f32 v83, v112, v113
	v_perm_b32 v145, v83, v82, s86
	v_mfma_scale_f32_16x16x128_f8f6f4 v[190:193], v[122:129], v[114:121], v[190:193], v227, v227 op_sel_hi:[0,0,0] cbsz:1
	s_setprio 1
	v_mfma_scale_f32_32x32x64_f8f6f4 v[82:97], v[194:197], v[178:181], v[2:17], v229, v228 op_sel_hi:[0,0,0] cbsz:4 blgp:4
	v_mfma_scale_f32_32x32x64_f8f6f4 v[98:113], v[198:201], v[178:181], v[2:17], v229, v228 op_sel_hi:[0,0,0] cbsz:4 blgp:4
	s_nop 0
	v_mfma_scale_f32_32x32x64_f8f6f4 v[82:97], v[202:205], v[182:185], v[82:97], v229, v228 op_sel_hi:[0,0,0] cbsz:4 blgp:4
	v_mfma_scale_f32_32x32x64_f8f6f4 v[98:113], v[206:209], v[182:185], v[98:113], v229, v228 op_sel_hi:[0,0,0] cbsz:4 blgp:4
	v_mfma_scale_f32_32x32x64_f8f6f4 v[34:49], v[130:137], v[154:161], v[34:49], v227, v227 op_sel_hi:[0,0,0] cbsz:1
	s_setprio 0
	s_nop 15
	s_nop 15
	s_nop 0
	v_cvt_pknorm_u16_f32 v82, v82, v83
	v_cvt_pknorm_u16_f32 v83, v84, v85
	v_perm_b32 v146, v83, v82, s86
	v_cvt_pknorm_u16_f32 v82, v98, v99
	v_cvt_pknorm_u16_f32 v83, v100, v101
	v_perm_b32 v150, v83, v82, s86
	v_cvt_pknorm_u16_f32 v82, v86, v87
	v_cvt_pknorm_u16_f32 v83, v88, v89
	v_perm_b32 v147, v83, v82, s86
	v_cvt_pknorm_u16_f32 v82, v102, v103
	v_cvt_pknorm_u16_f32 v83, v104, v105
	v_perm_b32 v151, v83, v82, s86
	v_mfma_scale_f32_32x32x64_f8f6f4 v[18:33], v[130:137], v[162:169], v[18:33], v227, v227 op_sel_hi:[0,0,0] cbsz:1
	s_add_i32 s11, s30, 0xffffc000
	s_and_b32 s11, s11, 0x6000
	v_add_u32_e32 v82, s11, v211
	ds_read_b128 v[194:197], v82
	ds_read_b128 v[198:201], v82 offset:512
	ds_read_b128 v[206:209], v82 offset:2048
	ds_read_b128 v[202:205], v82 offset:2560
	v_cvt_pknorm_u16_f32 v82, v90, v91
	v_cvt_pknorm_u16_f32 v83, v92, v93
	v_perm_b32 v148, v83, v82, s86
	v_cvt_pknorm_u16_f32 v82, v106, v107
	v_cvt_pknorm_u16_f32 v83, v108, v109
	v_perm_b32 v152, v83, v82, s86
	v_cvt_pknorm_u16_f32 v82, v94, v95
	v_cvt_pknorm_u16_f32 v83, v96, v97
	v_perm_b32 v149, v83, v82, s86
	v_cvt_pknorm_u16_f32 v82, v110, v111
	v_cvt_pknorm_u16_f32 v83, v112, v113
	v_perm_b32 v153, v83, v82, s86
	v_mfma_scale_f32_16x16x128_f8f6f4 v[186:189], v[130:137], v[114:121], v[186:189], v227, v227 op_sel_hi:[0,0,0] cbsz:1
	s_min_i32 s11, s8, 0x83
	s_sub_i32 s12, s11, s28
	s_ashr_i32 s13, s12, 31
	s_waitcnt vmcnt(2) lgkmcnt(0)
	s_barrier
	s_lshl_b64 s[12:13], s[12:13], 15
	s_add_i32 s10, s10, s29
	v_lshl_add_u64 v[82:83], v[214:215], 0, s[12:13]
	s_mov_b32 m0, s10
	s_nop 0
	global_load_lds_dwordx4 v[82:83], off
	s_add_i32 s10, s8, -2
	s_min_i32 s10, s10, 0x83
	s_sub_i32 s10, s10, s28
	s_ashr_i32 s11, s10, 31
	s_lshl_b64 s[10:11], s[10:11], 6
	v_lshl_add_u64 v[82:83], v[212:213], 0, s[10:11]
	s_add_i32 s9, s9, s31
	s_mov_b32 m0, s9
	s_nop 0
	global_load_lds_dwordx4 v[82:83], off
	s_add_i32 s8, s8, 2
	s_addk_i32 s30, 0x2000
	s_cmp_eq_u32 s30, 0x8a000
	s_cbranch_scc0 .LBB0_739
	ds_read_b128 v[82:85], v244 offset:45056
	ds_read_b128 v[90:93], v244 offset:45568
	ds_read_b128 v[86:89], v244 offset:46080
	ds_read_b128 v[94:97], v244 offset:46592
	s_waitcnt lgkmcnt(1)
	v_mfma_scale_f32_32x32x64_f8f6f4 v[50:65], v[138:145], v[82:89], v[50:65], v227, v227 op_sel_hi:[0,0,0] cbsz:1
	s_waitcnt lgkmcnt(0)
	v_mfma_scale_f32_32x32x64_f8f6f4 v[66:81], v[138:145], v[90:97], v[66:81], v227, v227 op_sel_hi:[0,0,0] cbsz:1
	v_mfma_scale_f32_16x16x128_f8f6f4 v[190:193], v[138:145], v[114:121], v[190:193], v227, v227 op_sel_hi:[0,0,0] cbsz:1
	v_mfma_scale_f32_32x32x64_f8f6f4 v[34:49], v[146:153], v[82:89], v[34:49], v227, v227 op_sel_hi:[0,0,0] cbsz:1
	v_mfma_scale_f32_32x32x64_f8f6f4 v[18:33], v[146:153], v[90:97], v[18:33], v227, v227 op_sel_hi:[0,0,0] cbsz:1
	v_mfma_scale_f32_16x16x128_f8f6f4 v[186:189], v[146:153], v[114:121], v[186:189], v227, v227 op_sel_hi:[0,0,0] cbsz:1
	v_and_b32_e32 v82, 7, v217
	s_nop 15
	s_nop 15
	s_nop 15
	s_nop 15
	s_waitcnt vmcnt(0) lgkmcnt(0)
	s_barrier
	s_lshl_b32 s8, s27, 11
	v_cmp_eq_u32_e32 vcc, 0, v82
	v_lshlrev_b32_e32 v82, 3, v217
	s_add_i32 s10, s15, s8
	v_and_b32_e32 v82, 64, v82
	v_and_b32_e32 v83, 48, v217
	v_add3_u32 v86, s10, v82, v83
	s_and_saveexec_b64 s[8:9], vcc
	ds_write_b128 v86, v[190:193]
	s_or_b64 exec, exec, s[8:9]
	s_waitcnt lgkmcnt(0)
	v_add_u32_e32 v85, s10, v210
	ds_read_b128 v[88:91], v85
	ds_read_b128 v[92:95], v85 offset:32
	v_add_u32_e32 v87, s10, v225
	v_lshlrev_b32_e32 v96, 8, v226
	s_add_u32 s4, s24, s4
	s_waitcnt lgkmcnt(1)
	v_rcp_f32_e32 v88, v88
	s_addc_u32 s5, s25, s5
	v_lshrrev_b32_e32 v83, 1, v224
	v_lshlrev_b32_e32 v82, 5, v217
	v_mul_f32_e32 v97, v50, v88
	v_rcp_f32_e32 v50, v89
	v_mul_f32_e32 v66, v66, v88
	s_add_u32 s8, s4, s7
	v_lshl_add_u32 v84, v83, 6, s10
	v_mul_f32_e32 v88, v51, v50
	v_mul_f32_e32 v67, v67, v50
	v_rcp_f32_e32 v50, v90
	v_and_b32_e32 v82, 32, v82
	s_addc_u32 s9, s5, 0
	s_ashr_i32 s7, s6, 31
	v_mul_f32_e32 v89, v52, v50
	v_mul_f32_e32 v68, v68, v50
	v_rcp_f32_e32 v50, v91
	s_lshl_b64 s[4:5], s[6:7], 9
	s_add_u32 s6, s8, s4
	v_lshlrev_b32_e32 v218, 9, v83
	v_mul_f32_e32 v90, v53, v50
	v_mul_f32_e32 v69, v69, v50
	s_waitcnt lgkmcnt(0)
	v_rcp_f32_e32 v50, v92
	s_addc_u32 s7, s9, s5
	v_mov_b32_e32 v83, v219
	v_mul_f32_e32 v91, v54, v50
	v_mul_f32_e32 v70, v70, v50
	v_rcp_f32_e32 v50, v93
	s_nop 0
	v_mul_f32_e32 v92, v55, v50
	v_mul_f32_e32 v71, v71, v50
	v_rcp_f32_e32 v50, v94
	s_nop 0
	v_mul_f32_e32 v93, v56, v50
	v_mul_f32_e32 v72, v72, v50
	v_rcp_f32_e32 v50, v95
	s_nop 0
	v_mul_f32_e32 v94, v57, v50
	v_mul_f32_e32 v73, v73, v50
	ds_read_b128 v[50:53], v85 offset:64
	ds_read_b128 v[54:57], v85 offset:96
	s_waitcnt lgkmcnt(0)
	s_waitcnt lgkmcnt(1)
	v_rcp_f32_e32 v50, v50
	s_nop 0
	v_mul_f32_e32 v58, v58, v50
	v_mul_f32_e32 v74, v74, v50
	v_rcp_f32_e32 v50, v51
	s_nop 0
	v_mul_f32_e32 v59, v59, v50
	v_mul_f32_e32 v75, v75, v50
	v_rcp_f32_e32 v50, v52
	s_nop 0
	v_mul_f32_e32 v60, v60, v50
	v_mul_f32_e32 v76, v76, v50
	v_rcp_f32_e32 v50, v53
	s_nop 0
	v_mul_f32_e32 v51, v61, v50
	v_mul_f32_e32 v52, v77, v50
	s_waitcnt lgkmcnt(0)
	v_rcp_f32_e32 v50, v54
	s_nop 0
	v_mul_f32_e32 v53, v62, v50
	v_mul_f32_e32 v54, v78, v50
	v_rcp_f32_e32 v50, v55
	s_nop 0
	v_mul_f32_e32 v55, v63, v50
	v_mul_f32_e32 v61, v79, v50
	v_rcp_f32_e32 v50, v56
	s_nop 0
	v_mul_f32_e32 v56, v64, v50
	v_mov_b32_e32 v64, v219
	v_cvt_pk_fp8_f32 v64, v97, v66
	v_mul_f32_e32 v62, v80, v50
	v_rcp_f32_e32 v50, v57
	v_cvt_pk_fp8_f32 v64, 0, 0 op_sel:[0,0,1]
	v_mul_f32_e32 v57, v65, v50
	v_mul_f32_e32 v63, v81, v50
	v_add_u32_e32 v50, v87, v96
	ds_write_b8 v50, v64
	v_lshrrev_b32_e32 v64, 8, v64
	ds_write_b8 v50, v64 offset:32
	v_mov_b32_e32 v64, v219
	v_cvt_pk_fp8_f32 v64, v88, v67
	v_cvt_pk_fp8_f32 v64, 0, 0 op_sel:[0,0,1]
	ds_write_b8 v50, v64 offset:64
	v_lshrrev_b32_e32 v64, 8, v64
	ds_write_b8 v50, v64 offset:96
	v_mov_b32_e32 v64, v219
	v_cvt_pk_fp8_f32 v64, v89, v68
	v_cvt_pk_fp8_f32 v64, 0, 0 op_sel:[0,0,1]
	ds_write_b8 v50, v64 offset:128
	v_lshrrev_b32_e32 v64, 8, v64
	ds_write_b8 v50, v64 offset:160
	v_mov_b32_e32 v64, v219
	v_cvt_pk_fp8_f32 v64, v90, v69
	v_cvt_pk_fp8_f32 v64, 0, 0 op_sel:[0,0,1]
	ds_write_b8 v50, v64 offset:192
	v_lshrrev_b32_e32 v64, 8, v64
	ds_write_b8 v50, v64 offset:224
	v_mov_b32_e32 v64, v219
	v_cvt_pk_fp8_f32 v64, v91, v70
	v_cvt_pk_fp8_f32 v64, 0, 0 op_sel:[0,0,1]
	ds_write_b8 v50, v64 offset:512
	v_lshrrev_b32_e32 v64, 8, v64
	ds_write_b8 v50, v64 offset:544
	v_mov_b32_e32 v64, v219
	v_cvt_pk_fp8_f32 v64, v92, v71
	v_cvt_pk_fp8_f32 v64, 0, 0 op_sel:[0,0,1]
	ds_write_b8 v50, v64 offset:576
	v_lshrrev_b32_e32 v64, 8, v64
	ds_write_b8 v50, v64 offset:608
	v_mov_b32_e32 v64, v219
	v_cvt_pk_fp8_f32 v64, v93, v72
	v_cvt_pk_fp8_f32 v64, 0, 0 op_sel:[0,0,1]
	ds_write_b8 v50, v64 offset:640
	v_lshrrev_b32_e32 v64, 8, v64
	ds_write_b8 v50, v64 offset:672
	v_mov_b32_e32 v64, v219
	v_cvt_pk_fp8_f32 v64, v94, v73
	v_cvt_pk_fp8_f32 v64, 0, 0 op_sel:[0,0,1]
	ds_write_b8 v50, v64 offset:704
	v_lshrrev_b32_e32 v64, 8, v64
	ds_write_b8 v50, v64 offset:736
	v_mov_b32_e32 v64, v219
	v_cvt_pk_fp8_f32 v64, v58, v74
	v_cvt_pk_fp8_f32 v64, 0, 0 op_sel:[0,0,1]
	s_nop 0
	v_lshrrev_b32_e32 v58, 8, v64
	ds_write_b8 v50, v58 offset:1056
	v_mov_b32_e32 v58, v219
	v_cvt_pk_fp8_f32 v58, v59, v75
	ds_write_b8 v50, v64 offset:1024
	v_cvt_pk_fp8_f32 v58, 0, 0 op_sel:[0,0,1]
	ds_write_b8 v50, v58 offset:1088
	v_lshrrev_b32_e32 v58, 8, v58
	ds_write_b8 v50, v58 offset:1120
	v_mov_b32_e32 v58, v219
	v_cvt_pk_fp8_f32 v58, v60, v76
	v_cvt_pk_fp8_f32 v58, 0, 0 op_sel:[0,0,1]
	ds_write_b8 v50, v58 offset:1152
	v_lshrrev_b32_e32 v58, 8, v58
	ds_write_b8 v50, v58 offset:1184
	v_mov_b32_e32 v58, v219
	v_cvt_pk_fp8_f32 v58, v51, v52
	v_cvt_pk_fp8_f32 v58, 0, 0 op_sel:[0,0,1]
	s_nop 0
	v_lshrrev_b32_e32 v51, 8, v58
	ds_write_b8 v50, v51 offset:1248
	v_mov_b32_e32 v51, v219
	v_cvt_pk_fp8_f32 v51, v53, v54
	ds_write_b8 v50, v58 offset:1216
	v_cvt_pk_fp8_f32 v51, 0, 0 op_sel:[0,0,1]
	ds_write_b8 v50, v51 offset:1536
	v_lshrrev_b32_e32 v51, 8, v51
	ds_write_b8 v50, v51 offset:1568
	v_mov_b32_e32 v51, v219
	v_cvt_pk_fp8_f32 v51, v55, v61
	v_lshl_add_u64 v[60:61], s[6:7], 0, v[218:219]
	v_lshl_add_u64 v[60:61], v[60:61], 0, v[82:83]
	v_cvt_pk_fp8_f32 v51, 0, 0 op_sel:[0,0,1]
	ds_write_b8 v50, v51 offset:1600
	v_lshrrev_b32_e32 v51, 8, v51
	ds_write_b8 v50, v51 offset:1632
	v_mov_b32_e32 v51, v219
	v_cvt_pk_fp8_f32 v51, v56, v62
	v_cvt_pk_fp8_f32 v51, 0, 0 op_sel:[0,0,1]
	ds_write_b8 v50, v51 offset:1664
	v_lshrrev_b32_e32 v51, 8, v51
	ds_write_b8 v50, v51 offset:1696
	v_mov_b32_e32 v51, v219
	v_cvt_pk_fp8_f32 v51, v57, v63
	v_cvt_pk_fp8_f32 v51, 0, 0 op_sel:[0,0,1]
	ds_write_b8 v50, v51 offset:1728
	v_lshrrev_b32_e32 v51, 8, v51
	ds_write_b8 v50, v51 offset:1760
	s_waitcnt lgkmcnt(0)
	v_add_u32_e32 v51, v84, v82
	ds_read_b128 v[52:55], v51
	ds_read_b128 v[56:59], v51 offset:16
	s_waitcnt lgkmcnt(1)
	global_store_dwordx4 v[60:61], v[52:55], off
	s_waitcnt lgkmcnt(0)
	global_store_dwordx4 v[60:61], v[56:59], off offset:16
	s_and_saveexec_b64 s[6:7], vcc
	s_cbranch_execz .LBB0_737
	ds_write_b128 v86, v[186:189]
	s_branch .LBB0_737

.LBB0_747:
	s_ashr_i32 s2, s16, 3
	s_mul_i32 s21, s2, 0x420000
	s_mul_hi_i32 s3, s2, 0x420000
	s_add_u32 s2, s8, s21
	s_addc_u32 s5, s9, s3
	s_and_b32 s22, s19, 0x1c0
	s_add_u32 s4, s2, s22
	s_addc_u32 s5, s5, 0
	s_add_u32 s2, s10, s21
	s_addc_u32 s6, s11, s3
	v_mov_b32_e32 v115, v0
	s_add_u32 s24, s2, s22
	s_addc_u32 s25, s6, 0
	v_readfirstlane_b32 s2, v115
	s_ashr_i32 s28, s2, 8
	s_ashr_i32 s23, s2, 6
	s_lshl_b32 s2, s28, 12
	v_and_b32_e32 v116, 31, v115
	s_add_i32 s27, s2, s15
	s_lshl_b32 s2, s23, 5
	v_or_b32_e32 v18, s2, v116
	v_ashrrev_i32_e32 v19, 31, v18
	v_bfe_u32 v117, v115, 5, 1
	v_lshlrev_b64 v[18:19], 9, v[18:19]
	v_lshl_add_u64 v[18:19], s[4:5], 0, v[18:19]
	v_lshlrev_b32_e32 v218, 4, v117
	s_lshl_b32 s7, s28, 6
	v_lshl_add_u64 v[18:19], v[18:19], 0, v[218:219]
	v_and_b32_e32 v114, 63, v115
	s_and_b32 s6, s23, 3
	global_load_dwordx4 v[102:105], v[18:19], off
	s_waitcnt vmcnt(0)
	global_load_dwordx4 v[98:101], v[18:19], off offset:32
	v_mov_b32_e32 v18, s7
	s_movk_i32 s4, 0x2100
	v_mad_u32_u24 v18, v114, s4, v18
	s_lshl_b32 s4, s6, 10
	s_add_i32 s29, s4, s27
	s_min_i32 s4, s28, 3
	s_lshl_b32 s26, s6, 4
	s_sub_i32 s6, s4, s28
	v_or_b32_e32 v20, s7, v114
	s_ashr_i32 s7, s6, 31
	s_lshl_b64 s[4:5], s[6:7], 6
	s_lshl_b64 s[6:7], s[6:7], 15
	s_add_u32 s6, s24, s6
	v_lshl_or_b32 v112, v20, 9, s26
	s_addc_u32 s7, s25, s7
	v_mov_b32_e32 v113, v219
	s_waitcnt vmcnt(0)
	v_or_b32_e32 v110, s26, v18
	v_lshl_add_u64 v[18:19], s[6:7], 0, v[112:113]
	s_mov_b32 m0, s29
	s_nop 0
	global_load_lds_dwordx4 v[18:19], off
	s_min_i32 s6, s28, 1
	s_sub_i32 s6, s6, s28
	s_add_i32 s6, s6, 2
	s_ashr_i32 s7, s6, 31
	s_lshl_b64 s[30:31], s[6:7], 6
	s_lshl_b64 s[6:7], s[6:7], 15
	s_add_u32 s6, s24, s6
	s_addc_u32 s7, s25, s7
	s_add_i32 s27, s29, 0x2000
	s_add_u32 s4, s17, s4
	v_mov_b32_e32 v111, v219
	v_lshl_add_u64 v[18:19], s[6:7], 0, v[112:113]
	s_mov_b32 m0, s27
	s_nop 0
	global_load_lds_dwordx4 v[18:19], off
	s_addc_u32 s5, s18, s5
	v_lshl_add_u64 v[18:19], s[4:5], 0, v[110:111]
	s_add_i32 s26, s29, 0x8000
	s_mov_b32 m0, s26
	s_nop 0
	global_load_lds_dwordx4 v[18:19], off
	s_min_i32 s4, s28, -1
	s_sub_i32 s4, s4, s28
	s_add_i32 s6, s4, 4
	s_ashr_i32 s7, s6, 31
	s_lshl_b64 s[4:5], s[6:7], 15
	s_add_u32 s4, s24, s4
	s_addc_u32 s5, s25, s5
	v_lshl_add_u64 v[18:19], s[4:5], 0, v[112:113]
	s_add_i32 s4, s29, 0x4000
	s_mov_b32 m0, s4
	s_nop 0
	global_load_lds_dwordx4 v[18:19], off
	s_add_u32 s4, s17, s30
	s_addc_u32 s5, s18, s31
	v_lshl_add_u64 v[18:19], s[4:5], 0, v[110:111]
	s_add_i32 s4, s29, 0xa000
	s_mov_b32 m0, s4
	s_nop 0
	global_load_lds_dwordx4 v[18:19], off
	s_min_i32 s4, s28, -3
	s_sub_i32 s4, s4, s28
	s_add_i32 s30, s4, 6
	s_ashr_i32 s31, s30, 31
	s_lshl_b64 s[4:5], s[30:31], 6
	s_lshl_b64 s[30:31], s[30:31], 15
	v_lshrrev_b32_e32 v18, 4, v115
	v_lshrrev_b32_e32 v19, 3, v115
	s_add_u32 s30, s24, s30
	v_lshlrev_b32_e32 v21, 10, v117
	v_lshlrev_b32_e32 v66, 4, v116
	v_bitop3_b32 v18, v18, 1, v19 bitop3:0x48
	s_addc_u32 s31, s25, s31
	v_add3_u32 v118, s15, v21, v66
	v_cmp_eq_u32_e32 vcc, 0, v18
	s_waitcnt vmcnt(2) lgkmcnt(0)
	s_barrier
	v_lshl_add_u64 v[18:19], s[30:31], 0, v[112:113]
	s_add_i32 s30, s29, 0x6000
	s_lshl_b64 s[6:7], s[6:7], 6
	ds_read_b128 v[50:53], v118
	ds_read_b128 v[58:61], v118 offset:2048
	ds_read_b128 v[54:57], v118 offset:512
	ds_read_b128 v[62:65], v118 offset:2560
	s_waitcnt lgkmcnt(0)
	s_barrier
	s_add_u32 s6, s17, s6
	s_mov_b32 m0, s30
	s_nop 0
	global_load_lds_dwordx4 v[18:19], off
	s_addc_u32 s7, s18, s7
	v_lshl_add_u64 v[18:19], s[6:7], 0, v[110:111]
	s_add_i32 s6, s29, 0xc000
	s_mov_b32 m0, s6
	s_nop 0
	global_load_lds_dwordx4 v[18:19], off
	v_mov_b32_e32 v119, 0x7f7f7f7f
	v_mov_b32_e32 v120, 0x76767676
	v_mov_b32_e32 v121, 0x7e7e7e7e
	v_cndmask_b32_e32 v82, 0, v237, vcc
	v_lshlrev_b32_e32 v67, 11, v117
	s_waitcnt lgkmcnt(3)
	v_mfma_scale_f32_32x32x64_f8f6f4 v[34:49], v[50:53], v[102:105], v[2:17], v121, v120 op_sel_hi:[0,0,0] cbsz:4 blgp:4
	s_waitcnt lgkmcnt(1)
	v_mfma_scale_f32_32x32x64_f8f6f4 v[18:33], v[54:57], v[102:105], v[2:17], v121, v120 op_sel_hi:[0,0,0] cbsz:4 blgp:4
	v_mov_b32_e32 v83, v82
	v_mov_b32_e32 v84, v82
	v_mov_b32_e32 v85, v82
	v_mov_b32_e32 v86, v82
	v_mov_b32_e32 v87, v82
	v_mov_b32_e32 v88, v82
	v_mov_b32_e32 v89, v82
	v_mfma_scale_f32_32x32x64_f8f6f4 v[34:49], v[58:61], v[98:101], v[34:49], v121, v120 op_sel_hi:[0,0,0] cbsz:4 blgp:4
	s_waitcnt lgkmcnt(0)
	v_mfma_scale_f32_32x32x64_f8f6f4 v[18:33], v[62:65], v[98:101], v[18:33], v121, v120 op_sel_hi:[0,0,0] cbsz:4 blgp:4
	s_nop 0
	s_nop 15
	s_nop 15
	s_nop 0
	v_cvt_pknorm_u16_f32 v18, v18, v19
	v_cvt_pknorm_u16_f32 v19, v20, v21
	v_perm_b32 v94, v19, v18, s86
	v_cvt_pknorm_u16_f32 v18, v38, v39
	v_cvt_pknorm_u16_f32 v19, v40, v41
	v_perm_b32 v91, v19, v18, s86
	v_cvt_pknorm_u16_f32 v18, v22, v23
	v_cvt_pknorm_u16_f32 v19, v24, v25
	v_perm_b32 v95, v19, v18, s86
	v_cvt_pknorm_u16_f32 v18, v42, v43
	v_cvt_pknorm_u16_f32 v19, v44, v45
	v_perm_b32 v92, v19, v18, s86
	v_cvt_pknorm_u16_f32 v18, v26, v27
	v_cvt_pknorm_u16_f32 v19, v28, v29
	v_perm_b32 v96, v19, v18, s86
	v_cvt_pknorm_u16_f32 v18, v46, v47
	v_cvt_pknorm_u16_f32 v19, v48, v49
	v_cvt_pknorm_u16_f32 v34, v34, v35
	v_cvt_pknorm_u16_f32 v35, v36, v37
	v_perm_b32 v93, v19, v18, s86
	v_cvt_pknorm_u16_f32 v18, v30, v31
	v_cvt_pknorm_u16_f32 v19, v32, v33
	v_perm_b32 v90, v35, v34, s86
	v_perm_b32 v97, v19, v18, s86
	ds_read_b128 v[106:109], v118 offset:4096
	ds_read_b128 v[146:149], v118 offset:4608
	ds_read_b128 v[150:153], v118 offset:6144
	ds_read_b128 v[154:157], v118 offset:6656
	v_add3_u32 v162, s15, v67, v66
	s_setprio 1
	s_waitcnt lgkmcnt(3)
	v_mfma_scale_f32_32x32x64_f8f6f4 v[66:81], v[106:109], v[102:105], v[2:17], v121, v120 op_sel_hi:[0,0,0] cbsz:4 blgp:4
	s_waitcnt lgkmcnt(2)
	v_mfma_scale_f32_32x32x64_f8f6f4 v[50:65], v[146:149], v[102:105], v[2:17], v121, v120 op_sel_hi:[0,0,0] cbsz:4 blgp:4
	s_waitcnt lgkmcnt(1)
	v_mfma_scale_f32_32x32x64_f8f6f4 v[66:81], v[150:153], v[98:101], v[66:81], v121, v120 op_sel_hi:[0,0,0] cbsz:4 blgp:4
	s_waitcnt lgkmcnt(0)
	v_mfma_scale_f32_32x32x64_f8f6f4 v[50:65], v[154:157], v[98:101], v[50:65], v121, v120 op_sel_hi:[0,0,0] cbsz:4 blgp:4
	ds_read_b128 v[130:133], v162 offset:32768
	ds_read_b128 v[138:141], v162 offset:33280
	ds_read_b128 v[134:137], v162 offset:33792
	ds_read_b128 v[142:145], v162 offset:34304
	v_readlane_b32 s40, v255, 8
	v_readlane_b32 s41, v255, 9
	v_readlane_b32 s42, v255, 10
	v_readlane_b32 s43, v255, 11
	v_readlane_b32 s44, v255, 12
	v_readlane_b32 s45, v255, 13
	v_readlane_b32 s46, v255, 14
	v_readlane_b32 s47, v255, 15
	v_readlane_b32 s48, v255, 16
	v_readlane_b32 s49, v255, 17
	v_readlane_b32 s50, v255, 18
	v_readlane_b32 s51, v255, 19
	v_readlane_b32 s52, v255, 20
	v_readlane_b32 s53, v255, 21
	v_readlane_b32 s54, v255, 22
	v_readlane_b32 s55, v255, 23
	v_mov_b64_e32 v[18:19], s[40:41]
	v_mov_b64_e32 v[20:21], s[42:43]
	v_mov_b64_e32 v[32:33], s[54:55]
	v_mov_b64_e32 v[22:23], s[44:45]
	v_mov_b64_e32 v[24:25], s[46:47]
	v_mov_b64_e32 v[26:27], s[48:49]
	v_mov_b64_e32 v[28:29], s[50:51]
	v_mov_b64_e32 v[30:31], s[52:53]
	v_mov_b64_e32 v[48:49], v[32:33]
	v_mov_b64_e32 v[46:47], v[30:31]
	v_mov_b64_e32 v[44:45], v[28:29]
	v_mov_b64_e32 v[42:43], v[26:27]
	v_mov_b64_e32 v[40:41], v[24:25]
	v_mov_b64_e32 v[38:39], v[22:23]
	v_mov_b64_e32 v[36:37], v[20:21]
	v_mov_b64_e32 v[34:35], v[18:19]
	s_waitcnt lgkmcnt(1)
	v_mfma_scale_f32_32x32x64_f8f6f4 v[34:49], v[90:97], v[130:137], v[34:49], v119, v119 op_sel_hi:[0,0,0] cbsz:1
	s_setprio 0
	s_nop 15
	s_nop 15
	s_nop 0
	v_cvt_pknorm_u16_f32 v50, v50, v51
	v_cvt_pknorm_u16_f32 v51, v52, v53
	v_perm_b32 v126, v51, v50, s86
	v_cvt_pknorm_u16_f32 v50, v70, v71
	v_cvt_pknorm_u16_f32 v51, v72, v73
	v_cvt_pknorm_u16_f32 v66, v66, v67
	v_cvt_pknorm_u16_f32 v67, v68, v69
	v_perm_b32 v123, v51, v50, s86
	v_cvt_pknorm_u16_f32 v50, v54, v55
	v_cvt_pknorm_u16_f32 v51, v56, v57
	v_perm_b32 v122, v67, v66, s86
	v_perm_b32 v127, v51, v50, s86
	s_waitcnt lgkmcnt(0)
	v_mfma_scale_f32_32x32x64_f8f6f4 v[18:33], v[90:97], v[138:145], v[18:33], v119, v119 op_sel_hi:[0,0,0] cbsz:1
	ds_read_b128 v[146:149], v118 offset:8192
	ds_read_b128 v[150:153], v118 offset:8704
	ds_read_b128 v[154:157], v118 offset:10240
	ds_read_b128 v[158:161], v118 offset:10752
	v_cvt_pknorm_u16_f32 v50, v74, v75
	v_cvt_pknorm_u16_f32 v51, v76, v77
	v_perm_b32 v124, v51, v50, s86
	v_cvt_pknorm_u16_f32 v50, v58, v59
	v_cvt_pknorm_u16_f32 v51, v60, v61
	v_perm_b32 v128, v51, v50, s86
	v_cvt_pknorm_u16_f32 v50, v78, v79
	v_cvt_pknorm_u16_f32 v51, v80, v81
	v_perm_b32 v125, v51, v50, s86
	v_cvt_pknorm_u16_f32 v50, v62, v63
	v_cvt_pknorm_u16_f32 v51, v64, v65
	v_perm_b32 v129, v51, v50, s86
	v_mov_b32_e32 v106, v219
	v_mov_b32_e32 v107, v219
	v_mov_b32_e32 v108, v219
	v_mov_b32_e32 v109, v219
	v_mfma_scale_f32_16x16x128_f8f6f4 v[106:109], v[90:97], v[82:89], v[106:109], v119, v119 op_sel_hi:[0,0,0] cbsz:1
	s_min_i32 s6, s28, -5
	s_sub_i32 s6, s6, s28
	s_add_i32 s30, s6, 8
	s_ashr_i32 s31, s30, 31
	s_lshl_b64 s[6:7], s[30:31], 6
	s_lshl_b64 s[30:31], s[30:31], 15
	s_add_u32 s30, s24, s30
	s_addc_u32 s31, s25, s31
	s_add_u32 s4, s17, s4
	s_waitcnt vmcnt(2) lgkmcnt(0)
	s_barrier
	v_lshl_add_u64 v[50:51], s[30:31], 0, v[112:113]
	s_addc_u32 s5, s18, s5
	s_mov_b32 m0, s29
	s_nop 0
	global_load_lds_dwordx4 v[50:51], off
	v_lshl_add_u64 v[50:51], s[4:5], 0, v[110:111]
	s_add_i32 s4, s29, 0xe000
	s_mov_b32 m0, s4
	s_nop 0
	global_load_lds_dwordx4 v[50:51], off
	s_min_i32 s4, s28, -7
	s_sub_i32 s4, s4, s28
	s_ashr_i32 s5, s4, 31
	s_lshl_b64 s[4:5], s[4:5], 15
	s_setprio 1
	s_waitcnt lgkmcnt(3)
	v_mfma_scale_f32_32x32x64_f8f6f4 v[66:81], v[146:149], v[102:105], v[2:17], v121, v120 op_sel_hi:[0,0,0] cbsz:4 blgp:4
	s_waitcnt lgkmcnt(2)
	v_mfma_scale_f32_32x32x64_f8f6f4 v[50:65], v[150:153], v[102:105], v[2:17], v121, v120 op_sel_hi:[0,0,0] cbsz:4 blgp:4
	s_waitcnt lgkmcnt(1)
	v_mfma_scale_f32_32x32x64_f8f6f4 v[66:81], v[154:157], v[98:101], v[66:81], v121, v120 op_sel_hi:[0,0,0] cbsz:4 blgp:4
	s_waitcnt lgkmcnt(0)
	v_mfma_scale_f32_32x32x64_f8f6f4 v[50:65], v[158:161], v[98:101], v[50:65], v121, v120 op_sel_hi:[0,0,0] cbsz:4 blgp:4
	ds_read_b128 v[130:133], v162 offset:36864
	ds_read_b128 v[138:141], v162 offset:37376
	ds_read_b128 v[134:137], v162 offset:37888
	ds_read_b128 v[142:145], v162 offset:38400
	s_waitcnt lgkmcnt(1)
	v_mfma_scale_f32_32x32x64_f8f6f4 v[34:49], v[122:129], v[130:137], v[34:49], v119, v119 op_sel_hi:[0,0,0] cbsz:1
	s_setprio 0
	s_nop 15
	s_nop 15
	s_nop 0
	v_cvt_pknorm_u16_f32 v50, v50, v51
	v_cvt_pknorm_u16_f32 v51, v52, v53
	v_perm_b32 v94, v51, v50, s86
	v_cvt_pknorm_u16_f32 v50, v70, v71
	v_cvt_pknorm_u16_f32 v51, v72, v73
	v_cvt_pknorm_u16_f32 v66, v66, v67
	v_cvt_pknorm_u16_f32 v67, v68, v69
	v_perm_b32 v91, v51, v50, s86
	v_cvt_pknorm_u16_f32 v50, v54, v55
	v_cvt_pknorm_u16_f32 v51, v56, v57
	v_perm_b32 v90, v67, v66, s86
	v_perm_b32 v95, v51, v50, s86
	s_waitcnt lgkmcnt(0)
	v_mfma_scale_f32_32x32x64_f8f6f4 v[18:33], v[122:129], v[138:145], v[18:33], v119, v119 op_sel_hi:[0,0,0] cbsz:1
	ds_read_b128 v[146:149], v118 offset:12288
	ds_read_b128 v[150:153], v118 offset:12800
	ds_read_b128 v[154:157], v118 offset:14336
	ds_read_b128 v[158:161], v118 offset:14848
	v_cvt_pknorm_u16_f32 v50, v74, v75
	v_cvt_pknorm_u16_f32 v51, v76, v77
	v_perm_b32 v92, v51, v50, s86
	v_cvt_pknorm_u16_f32 v50, v58, v59
	v_cvt_pknorm_u16_f32 v51, v60, v61
	v_perm_b32 v96, v51, v50, s86
	v_cvt_pknorm_u16_f32 v50, v78, v79
	v_cvt_pknorm_u16_f32 v51, v80, v81
	v_perm_b32 v93, v51, v50, s86
	v_cvt_pknorm_u16_f32 v50, v62, v63
	v_cvt_pknorm_u16_f32 v51, v64, v65
	v_perm_b32 v97, v51, v50, s86
	v_mfma_scale_f32_16x16x128_f8f6f4 v[106:109], v[122:129], v[82:89], v[106:109], v119, v119 op_sel_hi:[0,0,0] cbsz:1
	s_setprio 1
	s_waitcnt lgkmcnt(3)
	v_mfma_scale_f32_32x32x64_f8f6f4 v[66:81], v[146:149], v[102:105], v[2:17], v121, v120 op_sel_hi:[0,0,0] cbsz:4 blgp:4
	s_waitcnt lgkmcnt(2)
	v_mfma_scale_f32_32x32x64_f8f6f4 v[50:65], v[150:153], v[102:105], v[2:17], v121, v120 op_sel_hi:[0,0,0] cbsz:4 blgp:4
	s_waitcnt lgkmcnt(1)
	v_mfma_scale_f32_32x32x64_f8f6f4 v[66:81], v[154:157], v[98:101], v[66:81], v121, v120 op_sel_hi:[0,0,0] cbsz:4 blgp:4
	s_waitcnt lgkmcnt(0)
	v_mfma_scale_f32_32x32x64_f8f6f4 v[50:65], v[158:161], v[98:101], v[50:65], v121, v120 op_sel_hi:[0,0,0] cbsz:4 blgp:4
	ds_read_b128 v[98:101], v162 offset:40960
	ds_read_b128 v[130:133], v162 offset:41472
	ds_read_b128 v[102:105], v162 offset:41984
	ds_read_b128 v[134:137], v162 offset:42496
	s_waitcnt lgkmcnt(1)
	v_mfma_scale_f32_32x32x64_f8f6f4 v[34:49], v[90:97], v[98:105], v[34:49], v119, v119 op_sel_hi:[0,0,0] cbsz:1
	s_setprio 0
	s_nop 15
	s_nop 15
	s_nop 0
	v_cvt_pknorm_u16_f32 v50, v50, v51
	v_cvt_pknorm_u16_f32 v51, v52, v53
	v_perm_b32 v124, v51, v50, s86
	v_cvt_pknorm_u16_f32 v50, v70, v71
	v_cvt_pknorm_u16_f32 v51, v72, v73
	v_cvt_pknorm_u16_f32 v66, v66, v67
	v_cvt_pknorm_u16_f32 v67, v68, v69
	v_perm_b32 v121, v51, v50, s86
	v_cvt_pknorm_u16_f32 v50, v54, v55
	v_cvt_pknorm_u16_f32 v51, v56, v57
	v_perm_b32 v120, v67, v66, s86
	v_perm_b32 v125, v51, v50, s86
	s_waitcnt lgkmcnt(0)
	v_mfma_scale_f32_32x32x64_f8f6f4 v[18:33], v[90:97], v[130:137], v[18:33], v119, v119 op_sel_hi:[0,0,0] cbsz:1
	v_cvt_pknorm_u16_f32 v50, v74, v75
	v_cvt_pknorm_u16_f32 v51, v76, v77
	v_perm_b32 v122, v51, v50, s86
	v_cvt_pknorm_u16_f32 v50, v58, v59
	v_cvt_pknorm_u16_f32 v51, v60, v61
	v_perm_b32 v126, v51, v50, s86
	v_cvt_pknorm_u16_f32 v50, v78, v79
	v_cvt_pknorm_u16_f32 v51, v80, v81
	v_perm_b32 v123, v51, v50, s86
	v_cvt_pknorm_u16_f32 v50, v62, v63
	v_cvt_pknorm_u16_f32 v51, v64, v65
	v_perm_b32 v127, v51, v50, s86
	v_mfma_scale_f32_16x16x128_f8f6f4 v[106:109], v[90:97], v[82:89], v[106:109], v119, v119 op_sel_hi:[0,0,0] cbsz:1
	s_add_u32 s4, s24, s4
	s_addc_u32 s5, s25, s5
	s_waitcnt vmcnt(2) lgkmcnt(0)
	s_barrier
	v_lshl_add_u64 v[50:51], s[4:5], 0, v[112:113]
	s_mov_b64 s[4:5], 0x50000
	v_lshl_add_u64 v[50:51], v[50:51], 0, s[4:5]
	s_mov_b32 m0, s27
	s_nop 0
	global_load_lds_dwordx4 v[50:51], off
	s_add_u32 s4, s17, s6
	s_addc_u32 s5, s18, s7
	v_lshl_add_u64 v[50:51], s[4:5], 0, v[110:111]
	s_mov_b32 m0, s26
	s_nop 0
	global_load_lds_dwordx4 v[50:51], off
	ds_read_b128 v[50:53], v162 offset:45056
	ds_read_b128 v[58:61], v162 offset:45568
	ds_read_b128 v[54:57], v162 offset:46080
	ds_read_b128 v[62:65], v162 offset:46592
	s_waitcnt lgkmcnt(1)
	v_mfma_scale_f32_32x32x64_f8f6f4 v[34:49], v[120:127], v[50:57], v[34:49], v119, v119 op_sel_hi:[0,0,0] cbsz:1
	s_waitcnt lgkmcnt(0)
	v_mfma_scale_f32_32x32x64_f8f6f4 v[18:33], v[120:127], v[58:65], v[18:33], v119, v119 op_sel_hi:[0,0,0] cbsz:1
	v_mfma_scale_f32_16x16x128_f8f6f4 v[106:109], v[120:127], v[82:89], v[106:109], v119, v119 op_sel_hi:[0,0,0] cbsz:1
	s_lshl_b32 s4, s23, 11
	s_nop 15
	s_nop 15
	s_waitcnt vmcnt(0) lgkmcnt(0)
	s_barrier
	v_and_b32_e32 v50, 7, v115
	s_add_i32 s6, s15, s4
	v_cmp_eq_u32_e32 vcc, 0, v50
	s_and_saveexec_b64 s[4:5], vcc
	s_cbranch_execz .LBB0_746
	v_lshlrev_b32_e32 v50, 3, v115
	v_and_b32_e32 v50, 64, v50
	v_and_b32_e32 v51, 48, v115
	v_add3_u32 v50, s6, v50, v51
	ds_write_b128 v50, v[106:109]
	s_branch .LBB0_746

.LBB0_757:
	s_bfe_u32 s10, s40, 0x40004
	s_and_b64 s[4:5], s[8:9], exec
	s_cselect_b32 s10, s10, s40
	s_ashr_i32 s4, s40, 4
	s_and_b32 s4, s4, -16
	s_and_b32 s5, s40, 15
	s_or_b32 s4, s5, s4
	s_add_i32 s14, s4, 1
	s_and_b64 s[4:5], s[8:9], exec
	s_cselect_b32 s18, s14, 0
	s_ashr_i32 s14, s10, 3
	s_ashr_i32 s19, s18, 31
	s_lshl_b64 s[4:5], s[18:19], 17
	s_mul_hi_i32 s15, s14, 0x420000
	s_mul_i32 s14, s14, 0x420000
	s_add_u32 s36, s4, s14
	s_addc_u32 s38, s5, s15
	s_add_u32 s4, s25, s36
	s_addc_u32 s5, s26, s38
	s_lshl_b32 s16, s10, 6
	s_and_b32 s33, s16, 0x1c0
	s_add_u32 s4, s4, s33
	s_addc_u32 s5, s5, 0
	s_add_u32 s14, s27, s14
	s_addc_u32 s15, s28, s15
	s_add_u32 s14, s14, s33
	s_addc_u32 s15, s15, 0
	s_mul_hi_i32 s17, s10, 0x84000
	s_mul_i32 s10, s10, 0x84000
	s_add_u32 s16, s29, s10
	s_addc_u32 s17, s30, s17
	s_and_b32 s10, s11, 3
	v_and_b32_e32 v246, 31, v244
	v_lshl_or_b32 v24, s10, 4, v18
	s_lshl_b32 s41, s10, 10
	s_lshl_b32 s10, s11, 5
	v_or_b32_e32 v18, s10, v246
	v_ashrrev_i32_e32 v19, 31, v18
	v_lshlrev_b64 v[18:19], 9, v[18:19]
	v_lshl_add_u64 v[18:19], s[4:5], 0, v[18:19]
	v_and_b32_e32 v218, 32, v244
	v_lshl_add_u64 v[18:19], v[18:19], 0, v[218:219]
	global_load_dwordx2 v[22:23], v[18:19], off offset:16
	s_nop 0
	global_load_dwordx4 v[18:21], v[18:19], off
	s_add_i32 s41, s41, s23
	v_cmp_gt_u32_e32 vcc, 32, v245
	v_cmp_lt_u32_e64 s[4:5], 31, v245
	v_mov_b32_e32 v218, v24
	s_add_i32 s42, s41, 0x8000
	v_lshl_add_u64 v[226:227], s[16:17], 0, v[218:219]
	s_waitcnt vmcnt(1)
	v_cndmask_b32_e32 v190, 0, v22, vcc
	s_waitcnt vmcnt(0)
	v_cndmask_b32_e32 v186, 0, v18, vcc
	v_cndmask_b32_e32 v187, 0, v19, vcc
	v_cndmask_b32_e32 v188, 0, v20, vcc
	v_cndmask_b32_e32 v189, 0, v21, vcc
	v_cndmask_b32_e32 v191, 0, v23, vcc
	v_cndmask_b32_e64 v192, 0, v18, s[4:5]
	v_cndmask_b32_e64 v193, 0, v19, s[4:5]
	v_cndmask_b32_e64 v194, 0, v20, s[4:5]
	v_cndmask_b32_e64 v195, 0, v21, s[4:5]
	v_cndmask_b32_e64 v196, 0, v22, s[4:5]
	v_cndmask_b32_e64 v197, 0, v23, s[4:5]
	s_mov_b64 s[4:5], -1
	s_and_b64 vcc, exec, s[12:13]
	s_cbranch_vccz .LBB0_759
	s_mov_b32 m0, s42
	s_nop 0
	global_load_lds_dwordx4 v[226:227], off
	s_mov_b64 s[4:5], 0
.LBB0_759:
	s_andn2_b64 vcc, exec, s[4:5]
	v_lshl_add_u64 v[228:229], s[14:15], 0, v[218:219]
	s_cbranch_vccnz .LBB0_761
	s_mov_b32 m0, s41
	s_nop 0
	global_load_lds_dwordx4 v[228:229], off
	v_lshl_add_u64 v[18:19], v[228:229], 0, s[68:69]
	s_add_i32 s4, s41, 0x1000
	s_mov_b32 m0, s4
	s_nop 0
	global_load_lds_dwordx4 v[18:19], off
	v_lshl_add_u64 v[18:19], v[228:229], 0, s[60:61]
	s_add_i32 s4, s41, 0x2000
	s_mov_b32 m0, s4
	s_nop 0
	global_load_lds_dwordx4 v[18:19], off
.LBB0_761:
	v_cndmask_b32_e64 v18, 0, 1, s[12:13]
	v_cmp_ne_u32_e64 s[4:5], 1, v18
	s_andn2_b64 vcc, exec, s[12:13]
	s_mov_b64 s[20:21], -1
	s_cbranch_vccnz .LBB0_763
	v_lshl_add_u64 v[18:19], v[226:227], 0, 64
	s_add_i32 s19, s42, 0x1000
	s_mov_b32 m0, s19
	s_nop 0
	global_load_lds_dwordx4 v[18:19], off
	s_mov_b64 s[20:21], 0
.LBB0_763:
	s_andn2_b64 vcc, exec, s[20:21]
	s_cbranch_vccnz .LBB0_765
	s_mov_b64 s[20:21], 0x18000
	v_lshl_add_u64 v[18:19], v[228:229], 0, s[20:21]
	s_add_i32 s19, s41, 0x3000
	s_mov_b32 m0, s19
	s_nop 0
	global_load_lds_dwordx4 v[18:19], off
.LBB0_765:
	s_cmp_eq_u32 s18, 0
	s_cselect_b32 s20, 3, 0x83
	s_and_b64 vcc, exec, s[4:5]
	s_mov_b64 s[18:19], -1
	s_cbranch_vccnz .LBB0_773
	v_lshl_add_u64 v[18:19], v[226:227], 0, s[72:73]
	s_add_i32 s18, s42, 0x2000
	s_mov_b32 m0, s18
	s_nop 0
	global_load_lds_dwordx4 v[18:19], off
	s_cbranch_execz .LBB0_774

.LBB0_768:
	s_mov_b64 s[18:19], 0xc0
	v_lshl_add_u64 v[18:19], v[226:227], 0, s[18:19]
	s_add_i32 s18, s42, 0x3000
	s_mov_b32 m0, s18
	s_nop 0
	global_load_lds_dwordx4 v[18:19], off
	s_cbranch_execz .LBB0_776

.LBB0_770:
	s_min_u32 s18, s20, 4
	s_lshl_b32 s18, s18, 6
	s_add_u32 s18, s16, s18
	s_addc_u32 s19, s17, 0
	v_lshl_add_u64 v[18:19], s[18:19], 0, v[218:219]
	s_add_i32 s18, s42, 0x4000
	s_mov_b32 m0, s18
	s_nop 0
	global_load_lds_dwordx4 v[18:19], off
	s_cbranch_execz .LBB0_778

.LBB0_772:
	s_min_u32 s4, s20, 5
	s_lshl_b32 s4, s4, 6
	s_add_u32 s4, s16, s4
	s_addc_u32 s5, s17, 0
	v_lshl_add_u64 v[18:19], s[4:5], 0, v[218:219]
	s_add_i32 s4, s42, 0x5000
	s_mov_b32 m0, s4
	s_nop 0
	global_load_lds_dwordx4 v[18:19], off
	s_cbranch_execz .LBB0_780
	s_branch .LBB0_781

.LBB0_774:
	s_min_u32 s18, s20, 4
	s_lshl_b32 s18, s18, 15
	s_add_u32 s18, s14, s18
	s_addc_u32 s19, s15, 0
	v_lshl_add_u64 v[18:19], s[18:19], 0, v[218:219]
	s_add_i32 s18, s41, 0x4000
	s_mov_b32 m0, s18
	s_nop 0
	global_load_lds_dwordx4 v[18:19], off
	s_and_b64 vcc, exec, s[4:5]
	s_mov_b64 s[18:19], -1
	s_cbranch_vccz .LBB0_768

.LBB0_776:
	s_min_u32 s18, s20, 5
	s_lshl_b32 s18, s18, 15
	s_add_u32 s18, s14, s18
	s_addc_u32 s19, s15, 0
	v_lshl_add_u64 v[18:19], s[18:19], 0, v[218:219]
	s_add_i32 s18, s41, 0x5000
	s_mov_b32 m0, s18
	s_nop 0
	global_load_lds_dwordx4 v[18:19], off
	s_and_b64 vcc, exec, s[4:5]
	s_mov_b64 s[18:19], -1
	s_cbranch_vccz .LBB0_770

.LBB0_778:
	s_min_u32 s18, s20, 6
	s_lshl_b32 s18, s18, 15
	s_add_u32 s18, s14, s18
	s_addc_u32 s19, s15, 0
	v_lshl_add_u64 v[18:19], s[18:19], 0, v[218:219]
	s_add_i32 s18, s41, 0x6000
	s_mov_b32 m0, s18
	s_nop 0
	global_load_lds_dwordx4 v[18:19], off
	s_and_b64 vcc, exec, s[4:5]
	s_mov_b64 s[4:5], -1
	s_cbranch_vccz .LBB0_772

.LBB0_780:
	s_min_u32 s4, s20, 7
	s_lshl_b32 s4, s4, 15
	s_add_u32 s4, s14, s4
	s_addc_u32 s5, s15, 0
	v_lshl_add_u64 v[18:19], s[4:5], 0, v[218:219]
	s_add_i32 s4, s41, 0x7000
	s_mov_b32 m0, s4
	s_nop 0
	global_load_lds_dwordx4 v[18:19], off
.LBB0_781:
	v_lshrrev_b32_e32 v247, 5, v245
	v_lshlrev_b32_e32 v18, 11, v247
	v_lshlrev_b32_e32 v19, 4, v246
	v_add3_u32 v249, s23, v18, v19
	s_waitcnt vmcnt(6) lgkmcnt(0)
	s_barrier
	ds_read_b128 v[50:53], v249
	ds_read2st64_b64 v[18:21], v249 offset0:2 offset1:3
	ds_read_b128 v[56:59], v249 offset:512
	s_waitcnt lgkmcnt(0)
	s_barrier
	s_mov_b64 s[4:5], -1
	s_and_b64 vcc, exec, s[12:13]
	s_cbranch_vccz .LBB0_783
	s_min_u32 s4, s20, 6
	s_lshl_b32 s4, s4, 6
	s_add_u32 s4, s16, s4
	s_addc_u32 s5, s17, 0
	v_lshl_add_u64 v[22:23], s[4:5], 0, v[218:219]
	s_add_i32 s4, s42, 0x6000
	s_mov_b32 m0, s4
	s_nop 0
	global_load_lds_dwordx4 v[22:23], off
	s_mov_b64 s[4:5], 0
.LBB0_783:
	s_andn2_b64 vcc, exec, s[4:5]
	s_cbranch_vccnz .LBB0_785
	s_min_u32 s4, s20, 8
	s_lshl_b32 s4, s4, 15
	s_add_u32 s4, s14, s4
	s_addc_u32 s5, s15, 0
	v_lshl_add_u64 v[22:23], s[4:5], 0, v[218:219]
	s_mov_b32 m0, s41
	s_nop 0
	global_load_lds_dwordx4 v[22:23], off
.LBB0_785:
	v_mov_b32_e32 v248, 0x7f7f7f7f
	v_mov_b32_e32 v250, 0x77777777
	v_mov_b32_e32 v251, 0x7e7e7e7e
	s_waitcnt lgkmcnt(1)
	v_mov_b32_e32 v54, v18
	v_mov_b32_e32 v55, v19
	v_mov_b32_e32 v60, v20
	v_mov_b32_e32 v61, v21
	s_nop 0
	v_mfma_scale_f32_32x32x64_f8f6f4 v[34:49], v[50:55], v[186:191], v[2:17], v251, v250 op_sel_hi:[0,0,0] cbsz:2 blgp:2
	s_waitcnt lgkmcnt(0)
	v_mfma_scale_f32_32x32x64_f8f6f4 v[18:33], v[56:61], v[186:191], v[2:17], v251, v250 op_sel_hi:[0,0,0] cbsz:2 blgp:2
	v_mfma_scale_f32_32x32x64_f8f6f4 v[98:113], v[50:55], v[192:197], v[2:17], v251, v250 op_sel_hi:[0,0,0] cbsz:2 blgp:2
	v_mfma_scale_f32_32x32x64_f8f6f4 v[82:97], v[56:61], v[192:197], v[2:17], v251, v250 op_sel_hi:[0,0,0] cbsz:2 blgp:2
	ds_read_b128 v[198:201], v249 offset:4096
	ds_read2st64_b64 v[114:117], v249 offset0:10 offset1:11
	ds_read_b128 v[204:207], v249 offset:4608
	s_nop 15
	s_nop 15
	s_nop 0
	v_cvt_pknorm_u16_f32 v18, v18, v19
	v_cvt_pknorm_u16_f32 v19, v20, v21
	v_perm_b32 v150, v19, v18, s86
	v_cvt_pknorm_u16_f32 v18, v38, v39
	v_cvt_pknorm_u16_f32 v19, v40, v41
	v_perm_b32 v147, v19, v18, s86
	v_cvt_pknorm_u16_f32 v18, v22, v23
	v_cvt_pknorm_u16_f32 v19, v24, v25
	v_perm_b32 v151, v19, v18, s86
	v_cvt_pknorm_u16_f32 v18, v42, v43
	v_cvt_pknorm_u16_f32 v19, v44, v45
	v_perm_b32 v148, v19, v18, s86
	v_cvt_pknorm_u16_f32 v18, v26, v27
	v_cvt_pknorm_u16_f32 v19, v28, v29
	v_perm_b32 v152, v19, v18, s86
	v_cvt_pknorm_u16_f32 v18, v46, v47
	v_cvt_pknorm_u16_f32 v19, v48, v49
	v_cvt_pknorm_u16_f32 v34, v34, v35
	v_cvt_pknorm_u16_f32 v35, v36, v37
	v_perm_b32 v149, v19, v18, s86
	v_cvt_pknorm_u16_f32 v18, v30, v31
	v_cvt_pknorm_u16_f32 v19, v32, v33
	v_perm_b32 v146, v35, v34, s86
	v_perm_b32 v153, v19, v18, s86
	s_waitcnt vmcnt(6) lgkmcnt(0)
	s_barrier
	s_mov_b64 s[4:5], -1
	s_and_b64 vcc, exec, s[12:13]
	s_cbranch_vccz .LBB0_787
	s_min_u32 s4, s20, 7
	s_lshl_b32 s4, s4, 6
	s_add_u32 s4, s16, s4
	s_addc_u32 s5, s17, 0
	v_lshl_add_u64 v[18:19], s[4:5], 0, v[218:219]
	s_add_i32 s4, s42, 0x7000
	s_mov_b32 m0, s4
	s_nop 0
	global_load_lds_dwordx4 v[18:19], off
	s_mov_b64 s[4:5], 0
.LBB0_787:
	s_andn2_b64 vcc, exec, s[4:5]
	s_cbranch_vccnz .LBB0_789
	s_min_u32 s4, s20, 9
	s_lshl_b32 s4, s4, 15
	s_add_u32 s4, s14, s4
	s_addc_u32 s5, s15, 0
	v_lshl_add_u64 v[18:19], s[4:5], 0, v[218:219]
	s_add_i32 s4, s41, 0x1000
	s_mov_b32 m0, s4
	s_nop 0
	global_load_lds_dwordx4 v[18:19], off

.LBB0_791:
	s_and_b32 s16, s15, 0x7000
	v_add_u32_e32 v114, s16, v249
	ds_read_b128 v[162:165], v114 offset:32768
	ds_read_b128 v[170:173], v114 offset:33280
	ds_read_b128 v[166:169], v114 offset:33792
	ds_read_b128 v[174:177], v114 offset:34304
	v_mfma_scale_f32_32x32x64_f8f6f4 v[114:129], v[198:203], v[186:191], v[2:17], v251, v250 op_sel_hi:[0,0,0] cbsz:2 blgp:2
	s_nop 0
	v_cvt_pknorm_u16_f32 v98, v98, v99
	v_cvt_pknorm_u16_f32 v99, v100, v101
	v_cvt_pknorm_u16_f32 v82, v82, v83
	v_cvt_pknorm_u16_f32 v83, v84, v85
	v_perm_b32 v178, v99, v98, s86
	v_perm_b32 v182, v83, v82, s86
	s_waitcnt lgkmcnt(4)
	v_mfma_scale_f32_32x32x64_f8f6f4 v[130:145], v[204:209], v[186:191], v[2:17], v251, v250 op_sel_hi:[0,0,0] cbsz:2 blgp:2
	s_cmp_eq_u32 s14, 0
	s_cbranch_scc1 .Lc_dma_done
	s_and_b64 vcc, exec, s[12:13]
	s_cbranch_vccz .Lc_dma_k
	s_add_i32 s4, s14, 7
	s_min_i32 s4, s4, s20
	s_lshl_b32 s58, s4, 6
	v_lshl_add_u64 v[84:85], v[226:227], 0, s[58:59]
	s_add_i32 s4, s15, 0xfffff000
	s_and_b32 s4, s4, 0x7000
	s_add_i32 s4, s4, s42
	s_mov_b32 m0, s4
	s_nop 0
	global_load_lds_dwordx4 v[84:85], off
	s_branch .Lc_dma_done
.Lc_dma_k:
	s_add_i32 s4, s14, 9
	s_min_i32 s4, s4, s20
	s_lshl_b32 s58, s4, 15
	v_lshl_add_u64 v[84:85], v[228:229], 0, s[58:59]
	s_add_i32 s4, s15, 0x1000
	s_and_b32 s4, s4, 0x7000
	s_add_i32 s4, s4, s41
	s_mov_b32 m0, s4
	s_nop 0
	global_load_lds_dwordx4 v[84:85], off
